# speedup vs baseline: 1.0182x; 1.0182x over previous
.Ledge_nosum:
	s_waitcnt lgkmcnt(0)
	s_barrier
	ds_read_b128 v[6:9], v176
	ds_read_b128 v[10:13], v176 offset:1024
	ds_read_b128 v[14:17], v176 offset:2048
	ds_read_b128 v[194:197], v176 offset:3072
	ds_read_b128 v[198:201], v189 offset:57344
	ds_read_b128 v[18:21], v189 offset:57360
	ds_read_b128 v[202:205], v176 offset:4096
	ds_read_b128 v[206:209], v176 offset:5120
	ds_read_b128 v[210:213], v176 offset:6144
	ds_read_b128 v[214:217], v176 offset:7168
	ds_read_b128 v[218:221], v189 offset:57408
	ds_read_b128 v[222:225], v189 offset:57424
	s_movk_i32 s0, 0x1200
	v_and_b32_e32 v188, 31, v0
	v_lshlrev_b32_e32 v226, 16, v2
	v_and_b32_e32 v227, 0xffff0000, v2
	v_lshlrev_b32_e32 v22, 16, v3
	v_and_b32_e32 v23, 0xffff0000, v3
	v_lshlrev_b32_e32 v2, 16, v4
	v_and_b32_e32 v3, 0xffff0000, v4
	v_lshlrev_b32_e32 v4, 16, v5
	v_and_b32_e32 v5, 0xffff0000, v5
	s_waitcnt lgkmcnt(0)
	v_pk_mul_f32 v[228:229], v[18:19], v[2:3]
	v_pk_mul_f32 v[18:19], v[20:21], v[4:5]
	v_pk_mul_f32 v[24:25], v[200:201], v[22:23]
	v_pk_mul_f32 v[26:27], v[198:199], v[226:227]
	v_cvt_pk_bf16_f32 v4, v228, v229
	v_pk_fma_f32 v[246:247], v[200:201], v[22:23], v[18:19]
	v_pk_fma_f32 v[248:249], v[198:199], v[226:227], v[228:229]
	ds_read_b128 v[198:201], v176 offset:8192
	ds_read_b128 v[226:229], v176 offset:9216
	ds_read_b128 v[230:233], v176 offset:10240
	ds_read_b128 v[234:237], v176 offset:11264
	ds_read_b128 v[238:241], v189 offset:57472
	ds_read_b128 v[242:245], v189 offset:57488
	v_cvt_pk_bf16_f32 v2, v26, v27
	v_cvt_pk_bf16_f32 v5, v18, v19
	v_cvt_pk_bf16_f32 v3, v24, v25
	s_nop 1
	v_mfma_f32_32x32x16_bf16 v[50:65], v[6:9], v[2:5], 0
	v_mfma_f32_32x32x16_bf16 v[34:49], v[10:13], v[2:5], 0
	v_mfma_f32_32x32x16_bf16 v[18:33], v[14:17], v[2:5], 0
	v_mfma_f32_32x32x16_bf16 v[2:17], v[194:197], v[2:5], 0
	v_lshlrev_b32_e32 v194, 16, v172
	v_and_b32_e32 v195, 0xffff0000, v172
	v_lshlrev_b32_e32 v172, 16, v173
	v_and_b32_e32 v173, 0xffff0000, v173
	v_lshlrev_b32_e32 v250, 16, v170
	v_and_b32_e32 v251, 0xffff0000, v170
	v_lshlrev_b32_e32 v170, 16, v171
	v_and_b32_e32 v171, 0xffff0000, v171
	v_pk_mul_f32 v[222:223], v[222:223], v[194:195]
	v_pk_mul_f32 v[172:173], v[224:225], v[172:173]
	v_pk_mul_f32 v[252:253], v[220:221], v[170:171]
	v_pk_mul_f32 v[254:255], v[218:219], v[250:251]
	v_cvt_pk_bf16_f32 v197, v172, v173
	v_pk_fma_f32 v[170:171], v[220:221], v[170:171], v[172:173]
	v_pk_fma_f32 v[172:173], v[218:219], v[250:251], v[222:223]
	v_cvt_pk_bf16_f32 v196, v222, v223
	v_cvt_pk_bf16_f32 v194, v254, v255
	v_cvt_pk_bf16_f32 v195, v252, v253
	v_pk_add_f32 v[172:173], v[248:249], v[172:173]
	v_pk_add_f32 v[170:171], v[246:247], v[170:171]
	v_mfma_f32_32x32x16_bf16 v[50:65], v[202:205], v[194:197], v[50:65]
	v_pk_mov_b32 v[202:203], v[172:173], v[170:171] op_sel:[1,0]
	v_mov_b32_e32 v173, v171
	v_pk_add_f32 v[170:171], v[202:203], v[172:173]
	s_nop 0
	v_pk_add_f32 v[170:171], v[170:171], v[170:171] op_sel:[0,1] op_sel_hi:[1,0]
	v_mfma_f32_32x32x16_bf16 v[34:49], v[206:209], v[194:197], v[34:49]
	v_mfma_f32_32x32x16_bf16 v[18:33], v[210:213], v[194:197], v[18:33]
	ds_read_b128 v[202:205], v176 offset:12288
	ds_read_b128 v[206:209], v176 offset:13312
	ds_read_b128 v[210:213], v176 offset:14336
	ds_read_b128 v[218:221], v176 offset:15360
	ds_read_b128 v[222:225], v189 offset:57536
	ds_read_b128 v[246:249], v189 offset:57552
	v_mfma_f32_32x32x16_bf16 v[2:17], v[214:217], v[194:197], v[2:17]
	v_lshlrev_b32_e32 v172, 16, v166
	v_and_b32_e32 v173, 0xffff0000, v166
	v_lshlrev_b32_e32 v194, 16, v167
	v_and_b32_e32 v195, 0xffff0000, v167
	v_lshlrev_b32_e32 v166, 16, v168
	v_and_b32_e32 v167, 0xffff0000, v168
	v_lshlrev_b32_e32 v168, 16, v169
	v_and_b32_e32 v169, 0xffff0000, v169
	s_waitcnt lgkmcnt(0)
	v_pk_mul_f32 v[196:197], v[240:241], v[194:195]
	v_pk_mul_f32 v[214:215], v[238:239], v[172:173]
	v_pk_mul_f32 v[216:217], v[242:243], v[166:167]
	v_pk_mul_f32 v[242:243], v[244:245], v[168:169]
	v_cvt_pk_bf16_f32 v168, v216, v217
	v_cvt_pk_bf16_f32 v166, v214, v215
	v_cvt_pk_bf16_f32 v169, v242, v243
	v_cvt_pk_bf16_f32 v167, v196, v197
	v_pk_fma_f32 v[194:195], v[240:241], v[194:195], v[242:243]
	v_pk_fma_f32 v[172:173], v[238:239], v[172:173], v[216:217]
	v_mfma_f32_32x32x16_bf16 v[50:65], v[198:201], v[166:169], v[50:65]
	v_mfma_f32_32x32x16_bf16 v[34:49], v[226:229], v[166:169], v[34:49]
	v_mfma_f32_32x32x16_bf16 v[18:33], v[230:233], v[166:169], v[18:33]
	v_mfma_f32_32x32x16_bf16 v[2:17], v[234:237], v[166:169], v[2:17]
	v_lshlrev_b32_e32 v166, 16, v164
	v_and_b32_e32 v167, 0xffff0000, v164
	v_lshlrev_b32_e32 v164, 16, v165
	v_and_b32_e32 v165, 0xffff0000, v165
	v_mul_f32_e64 v216, v248, v164
	v_mul_f32_e64 v217, v249, v165
	v_mul_u32_u24_e32 v164, 0x140, v192
	v_lshlrev_b32_e32 v164, 4, v164
	v_mov_b32_e32 v165, v175
	v_mul_u32_u24_e32 v171, 0x1400, v192
	v_lshl_add_u64 v[164:165], s[10:11], 0, v[164:165]
	v_readfirstlane_b32 s2, v171
	v_lshlrev_b32_e32 v196, 16, v162
	v_and_b32_e32 v197, 0xffff0000, v162
	v_lshlrev_b32_e32 v162, 16, v163
	v_and_b32_e32 v163, 0xffff0000, v163
	v_lshl_add_u64 v[164:165], v[164:165], 0, v[176:177]
	s_movk_i32 s1, 0x1400
	s_mov_b32 m0, s2
	v_mov_b32_e32 v171, 0x1000
	v_pk_mul_f32 v[198:199], v[224:225], v[162:163]
	s_waitcnt lgkmcnt(0)
	s_barrier
	global_load_lds_dwordx4 v[164:165], off
	global_load_lds_dwordx4 v[164:165], off offset:1024
	global_load_lds_dwordx4 v[164:165], off offset:2048
	global_load_lds_dwordx4 v[164:165], off offset:3072
	s_mov_b64 s[2:3], 0x1000
	v_mad_u32_u24 v171, v192, s1, v171
	v_pk_mul_f32 v[214:215], v[246:247], v[166:167]
	v_cvt_pk_bf16_f32 v167, v198, v199
	v_lshl_add_u64 v[198:199], v[164:165], 0, s[2:3]
	v_readfirstlane_b32 s2, v171
	s_mov_b32 m0, s2
	v_pk_mul_f32 v[200:201], v[222:223], v[196:197]
	global_load_lds_dwordx4 v[198:199], off
	v_pk_fma_f32 v[162:163], v[224:225], v[162:163], v[216:217]
	v_pk_fma_f32 v[196:197], v[222:223], v[196:197], v[214:215]
	v_pk_add_f32 v[162:163], v[194:195], v[162:163]
	v_pk_add_f32 v[172:173], v[172:173], v[196:197]
	v_cvt_pk_bf16_f32 v168, v214, v215
	v_cvt_pk_bf16_f32 v166, v200, v201
	v_cvt_pk_bf16_f32 v169, v216, v217
	v_pk_mov_b32 v[194:195], v[172:173], v[162:163] op_sel:[1,0]
	v_mov_b32_e32 v173, v163
	v_mfma_f32_32x32x16_bf16 v[50:65], v[202:205], v[166:169], v[50:65]
	v_add_f32_e64 v162, v194, v172
	v_add_f32_e64 v163, v195, v173
	v_pk_add_f32 v[162:163], v[162:163], v[162:163] op_sel:[0,1] op_sel_hi:[1,0]
	v_mfma_f32_32x32x16_bf16 v[34:49], v[206:209], v[166:169], v[34:49]
	v_mfma_f32_32x32x16_bf16 v[18:33], v[210:213], v[166:169], v[18:33]
	ds_read_b128 v[194:197], v176 offset:20480
	ds_read_b128 v[198:201], v176 offset:21504
	ds_read_b128 v[202:205], v176 offset:22528
	ds_read_b128 v[206:209], v176 offset:23552
	ds_read_b128 v[210:213], v189 offset:57600
	ds_read_b128 v[214:217], v189 offset:57616
	ds_read_b128 v[222:225], v176 offset:24576
	ds_read_b128 v[226:229], v176 offset:25600
	ds_read_b128 v[230:233], v176 offset:26624
	ds_read_b128 v[234:237], v176 offset:27648
	ds_read_b128 v[238:241], v189 offset:57664
	ds_read_b128 v[242:245], v189 offset:57680
	v_mfma_f32_32x32x16_bf16 v[2:17], v[218:221], v[166:169], v[2:17]
	v_lshlrev_b32_e32 v166, 16, v158
	v_and_b32_e32 v167, 0xffff0000, v158
	v_lshlrev_b32_e32 v168, 16, v159
	v_and_b32_e32 v169, 0xffff0000, v159
	v_lshlrev_b32_e32 v158, 16, v160
	v_and_b32_e32 v159, 0xffff0000, v160
	v_lshlrev_b32_e32 v160, 16, v161
	v_and_b32_e32 v161, 0xffff0000, v161
	s_waitcnt lgkmcnt(0)
	v_pk_mul_f32 v[172:173], v[212:213], v[168:169]
	v_pk_mul_f32 v[218:219], v[210:211], v[166:167]
	v_pk_mul_f32 v[214:215], v[214:215], v[158:159]
	v_pk_mul_f32 v[216:217], v[216:217], v[160:161]
	v_cvt_pk_bf16_f32 v160, v214, v215
	v_cvt_pk_bf16_f32 v158, v218, v219
	v_cvt_pk_bf16_f32 v161, v216, v217
	v_cvt_pk_bf16_f32 v159, v172, v173
	v_pk_fma_f32 v[172:173], v[212:213], v[168:169], v[216:217]
	v_pk_fma_f32 v[218:219], v[210:211], v[166:167], v[214:215]
	v_mfma_f32_32x32x16_bf16 v[50:65], v[194:197], v[158:161], v[50:65]
	v_mfma_f32_32x32x16_bf16 v[34:49], v[198:201], v[158:161], v[34:49]
	v_mfma_f32_32x32x16_bf16 v[18:33], v[202:205], v[158:161], v[18:33]
	ds_read_b128 v[166:169], v176 offset:28672
	ds_read_b128 v[194:197], v176 offset:29696
	ds_read_b128 v[198:201], v176 offset:30720
	ds_read_b128 v[202:205], v176 offset:31744
	ds_read_b128 v[210:213], v189 offset:57728
	ds_read_b128 v[214:217], v189 offset:57744
	v_mfma_f32_32x32x16_bf16 v[2:17], v[206:209], v[158:161], v[2:17]
	v_lshlrev_b32_e32 v206, 16, v154
	v_and_b32_e32 v207, 0xffff0000, v154
	v_lshlrev_b32_e32 v154, 16, v155
	v_and_b32_e32 v155, 0xffff0000, v155
	v_lshlrev_b32_e32 v158, 16, v156
	v_and_b32_e32 v159, 0xffff0000, v156
	v_lshlrev_b32_e32 v156, 16, v157
	v_and_b32_e32 v157, 0xffff0000, v157
	v_pk_mul_f32 v[208:209], v[240:241], v[154:155]
	v_pk_mul_f32 v[220:221], v[238:239], v[206:207]
	v_pk_mul_f32 v[242:243], v[242:243], v[158:159]
	v_pk_mul_f32 v[156:157], v[244:245], v[156:157]
	v_cvt_pk_bf16_f32 v160, v242, v243
	v_cvt_pk_bf16_f32 v158, v220, v221
	v_cvt_pk_bf16_f32 v161, v156, v157
	v_cvt_pk_bf16_f32 v159, v208, v209
	v_pk_fma_f32 v[154:155], v[240:241], v[154:155], v[156:157]
	v_pk_fma_f32 v[156:157], v[238:239], v[206:207], v[242:243]
	v_mfma_f32_32x32x16_bf16 v[50:65], v[222:225], v[158:161], v[50:65]
	v_add_f32_e64 v156, v218, v156
	v_add_f32_e64 v157, v219, v157
	v_add_f32_e64 v154, v172, v154
	v_add_f32_e64 v155, v173, v155
	v_pk_mov_b32 v[172:173], v[156:157], v[154:155] op_sel:[1,0]
	v_mov_b32_e32 v157, v155
	v_pk_add_f32 v[154:155], v[172:173], v[156:157]
	v_mfma_f32_32x32x16_bf16 v[34:49], v[226:229], v[158:161], v[34:49]
	v_add_f32_e64 v156, v154, v155
	v_add_f32_e64 v157, v155, v154
	v_mfma_f32_32x32x16_bf16 v[18:33], v[230:233], v[158:161], v[18:33]
	ds_read_b128 v[206:209], v176 offset:32768
	ds_read_b128 v[218:221], v176 offset:33792
	ds_read_b128 v[222:225], v176 offset:34816
	ds_read_b128 v[226:229], v176 offset:35840
	ds_read_b128 v[230:233], v189 offset:57792
	ds_read_b128 v[238:241], v189 offset:57808
	v_mfma_f32_32x32x16_bf16 v[2:17], v[234:237], v[158:161], v[2:17]
	v_lshlrev_b32_e32 v154, 16, v150
	v_and_b32_e32 v155, 0xffff0000, v150
	v_lshlrev_b32_e32 v158, 16, v151
	v_and_b32_e32 v159, 0xffff0000, v151
	v_lshlrev_b32_e32 v150, 16, v152
	v_and_b32_e32 v151, 0xffff0000, v152
	v_lshlrev_b32_e32 v152, 16, v153
	v_and_b32_e32 v153, 0xffff0000, v153
	s_waitcnt lgkmcnt(0)
	v_pk_mul_f32 v[160:161], v[212:213], v[158:159]
	v_pk_mul_f32 v[172:173], v[210:211], v[154:155]
	v_pk_mul_f32 v[214:215], v[214:215], v[150:151]
	v_pk_mul_f32 v[216:217], v[216:217], v[152:153]
	v_cvt_pk_bf16_f32 v152, v214, v215
	v_cvt_pk_bf16_f32 v150, v172, v173
	v_cvt_pk_bf16_f32 v153, v216, v217
	v_cvt_pk_bf16_f32 v151, v160, v161
	v_pk_fma_f32 v[158:159], v[212:213], v[158:159], v[216:217]
	v_pk_fma_f32 v[154:155], v[210:211], v[154:155], v[214:215]
	v_mfma_f32_32x32x16_bf16 v[50:65], v[166:169], v[150:153], v[50:65]
	v_mfma_f32_32x32x16_bf16 v[34:49], v[194:197], v[150:153], v[34:49]
	v_mfma_f32_32x32x16_bf16 v[18:33], v[198:201], v[150:153], v[18:33]
	v_mfma_f32_32x32x16_bf16 v[2:17], v[202:205], v[150:153], v[2:17]
	v_lshlrev_b32_e32 v152, 16, v146
	v_and_b32_e32 v153, 0xffff0000, v146
	v_lshlrev_b32_e32 v146, 16, v147
	v_and_b32_e32 v147, 0xffff0000, v147
	v_mov_b32_e32 v157, 0x5000
	v_lshlrev_b32_e32 v150, 16, v148
	v_and_b32_e32 v151, 0xffff0000, v148
	v_lshlrev_b32_e32 v148, 16, v149
	v_and_b32_e32 v149, 0xffff0000, v149
	v_pk_mul_f32 v[160:161], v[232:233], v[146:147]
	s_mov_b64 s[2:3], 0x5000
	v_mad_u32_u24 v157, v192, s1, v157
	v_pk_mul_f32 v[172:173], v[240:241], v[148:149]
	v_cvt_pk_bf16_f32 v149, v160, v161
	v_lshl_add_u64 v[160:161], v[164:165], 0, s[2:3]
	v_readfirstlane_b32 s2, v157
	s_mov_b32 m0, s2
	v_mov_b32_e32 v157, 0x6000
	s_waitcnt lgkmcnt(0)
	s_barrier
	global_load_lds_dwordx4 v[160:161], off
	global_load_lds_dwordx4 v[160:161], off offset:1024
	global_load_lds_dwordx4 v[160:161], off offset:2048
	global_load_lds_dwordx4 v[160:161], off offset:3072
	v_mad_u32_u24 v157, v192, s1, v157
	s_mov_b64 s[2:3], 0x6000
	v_readfirstlane_b32 s1, v157
	v_lshl_add_u64 v[160:161], v[164:165], 0, s[2:3]
	s_mov_b32 m0, s1
	v_pk_mul_f32 v[168:169], v[238:239], v[150:151]
	global_load_lds_dwordx4 v[160:161], off
	v_pk_mul_f32 v[166:167], v[230:231], v[152:153]
	v_pk_fma_f32 v[146:147], v[232:233], v[146:147], v[172:173]
	v_pk_fma_f32 v[152:153], v[230:231], v[152:153], v[168:169]
	v_pk_add_f32 v[146:147], v[158:159], v[146:147]
	v_pk_add_f32 v[152:153], v[154:155], v[152:153]
	v_cvt_pk_bf16_f32 v150, v168, v169
	v_cvt_pk_bf16_f32 v148, v166, v167
	v_cvt_pk_bf16_f32 v151, v172, v173
	v_pk_mov_b32 v[154:155], v[152:153], v[146:147] op_sel:[1,0]
	v_mov_b32_e32 v153, v147
	v_mfma_f32_32x32x16_bf16 v[50:65], v[206:209], v[148:151], v[50:65]
	v_add_f32_e64 v146, v154, v152
	v_add_f32_e64 v147, v155, v153
	v_pk_add_f32 v[146:147], v[146:147], v[146:147] op_sel:[0,1] op_sel_hi:[1,0]
	v_mfma_f32_32x32x16_bf16 v[34:49], v[218:221], v[148:151], v[34:49]
	v_mfma_f32_32x32x16_bf16 v[18:33], v[222:225], v[148:151], v[18:33]
	ds_read_b128 v[152:155], v176 offset:40960
	ds_read_b128 v[158:161], v176 offset:41984
	ds_read_b128 v[164:167], v176 offset:43008
	ds_read_b128 v[194:197], v176 offset:44032
	ds_read_b128 v[198:201], v189 offset:57856
	ds_read_b128 v[202:205], v189 offset:57872
	ds_read_b128 v[206:209], v176 offset:45056
	ds_read_b128 v[210:213], v176 offset:46080
	ds_read_b128 v[214:217], v176 offset:47104
	ds_read_b128 v[218:221], v176 offset:48128
	ds_read_b128 v[222:225], v189 offset:57920
	ds_read_b128 v[230:233], v189 offset:57936
	v_mfma_f32_32x32x16_bf16 v[2:17], v[226:229], v[148:151], v[2:17]
	v_lshlrev_b32_e32 v148, 16, v110
	v_and_b32_e32 v149, 0xffff0000, v110
	v_lshlrev_b32_e32 v150, 16, v111
	v_and_b32_e32 v151, 0xffff0000, v111
	v_lshlrev_b32_e32 v110, 16, v112
	v_and_b32_e32 v111, 0xffff0000, v112
	v_lshlrev_b32_e32 v112, 16, v113
	v_and_b32_e32 v113, 0xffff0000, v113
	s_waitcnt lgkmcnt(0)
	v_pk_mul_f32 v[168:169], v[200:201], v[150:151]
	v_pk_mul_f32 v[172:173], v[198:199], v[148:149]
	v_pk_mul_f32 v[202:203], v[202:203], v[110:111]
	v_pk_mul_f32 v[204:205], v[204:205], v[112:113]
	v_cvt_pk_bf16_f32 v112, v202, v203
	v_cvt_pk_bf16_f32 v110, v172, v173
	v_cvt_pk_bf16_f32 v113, v204, v205
	v_cvt_pk_bf16_f32 v111, v168, v169
	v_pk_fma_f32 v[148:149], v[198:199], v[148:149], v[202:203]
	s_nop 0
	v_mfma_f32_32x32x16_bf16 v[50:65], v[152:155], v[110:113], v[50:65]
	v_fma_f32 v154, v200, v150, v204
	v_fma_f32 v155, v201, v151, v205
	v_mfma_f32_32x32x16_bf16 v[34:49], v[158:161], v[110:113], v[34:49]
	v_mfma_f32_32x32x16_bf16 v[18:33], v[164:167], v[110:113], v[18:33]
	ds_read_b128 v[150:153], v176 offset:49152
	ds_read_b128 v[158:161], v176 offset:50176
	ds_read_b128 v[164:167], v176 offset:51200
	ds_read_b128 v[198:201], v176 offset:52224
	ds_read_b128 v[202:205], v189 offset:57984
	ds_read_b128 v[226:229], v189 offset:58000
	v_mfma_f32_32x32x16_bf16 v[2:17], v[194:197], v[110:113], v[2:17]
	v_lshlrev_b32_e32 v110, 16, v90
	v_and_b32_e32 v111, 0xffff0000, v90
	v_lshlrev_b32_e32 v112, 16, v91
	v_and_b32_e32 v113, 0xffff0000, v91
	v_lshlrev_b32_e32 v90, 16, v92
	v_and_b32_e32 v91, 0xffff0000, v92
	v_lshlrev_b32_e32 v92, 16, v93
	v_and_b32_e32 v93, 0xffff0000, v93
	v_pk_mul_f32 v[194:195], v[230:231], v[90:91]
	v_pk_mul_f32 v[196:197], v[232:233], v[92:93]
	v_pk_mul_f32 v[168:169], v[224:225], v[112:113]
	v_pk_mul_f32 v[172:173], v[222:223], v[110:111]
	v_pk_fma_f32 v[112:113], v[224:225], v[112:113], v[196:197]
	v_pk_fma_f32 v[110:111], v[222:223], v[110:111], v[194:195]
	v_pk_add_f32 v[112:113], v[154:155], v[112:113]
	v_pk_add_f32 v[110:111], v[148:149], v[110:111]
	v_cvt_pk_bf16_f32 v92, v194, v195
	v_pk_mov_b32 v[148:149], v[110:111], v[112:113] op_sel:[1,0]
	v_mov_b32_e32 v111, v113
	v_cvt_pk_bf16_f32 v90, v172, v173
	v_cvt_pk_bf16_f32 v93, v196, v197
	v_cvt_pk_bf16_f32 v91, v168, v169
	v_pk_add_f32 v[110:111], v[148:149], v[110:111]
	s_nop 0
	v_mfma_f32_32x32x16_bf16 v[50:65], v[206:209], v[90:93], v[50:65]
	v_add_f32_e64 v148, v110, v111
	v_add_f32_e64 v149, v111, v110
	v_mfma_f32_32x32x16_bf16 v[34:49], v[210:213], v[90:93], v[34:49]
	v_mfma_f32_32x32x16_bf16 v[18:33], v[214:217], v[90:93], v[18:33]
	ds_read_b128 v[110:113], v176 offset:53248
	ds_read_b128 v[194:197], v176 offset:54272
	ds_read_b128 v[206:209], v176 offset:55296
	ds_read_b128 v[210:213], v176 offset:56320
	ds_read_b128 v[214:217], v189 offset:58048
	ds_read_b128 v[222:225], v189 offset:58064
	v_mfma_f32_32x32x16_bf16 v[2:17], v[218:221], v[90:93], v[2:17]
	v_lshlrev_b32_e32 v90, 16, v86
	v_and_b32_e32 v91, 0xffff0000, v86
	v_lshlrev_b32_e32 v92, 16, v87
	v_and_b32_e32 v93, 0xffff0000, v87
	v_lshlrev_b32_e32 v86, 16, v88
	v_and_b32_e32 v87, 0xffff0000, v88
	v_lshlrev_b32_e32 v88, 16, v89
	v_and_b32_e32 v89, 0xffff0000, v89
	s_waitcnt lgkmcnt(0)
	v_pk_mul_f32 v[154:155], v[204:205], v[92:93]
	v_pk_mul_f32 v[168:169], v[202:203], v[90:91]
	v_pk_mul_f32 v[172:173], v[226:227], v[86:87]
	v_pk_mul_f32 v[218:219], v[228:229], v[88:89]
	v_cvt_pk_bf16_f32 v88, v172, v173
	v_cvt_pk_bf16_f32 v86, v168, v169
	v_cvt_pk_bf16_f32 v89, v218, v219
	v_cvt_pk_bf16_f32 v87, v154, v155
	v_pk_fma_f32 v[92:93], v[204:205], v[92:93], v[218:219]
	v_pk_fma_f32 v[90:91], v[202:203], v[90:91], v[172:173]
	v_mfma_f32_32x32x16_bf16 v[50:65], v[150:153], v[86:89], v[50:65]
	v_mfma_f32_32x32x16_bf16 v[34:49], v[158:161], v[86:89], v[34:49]
	v_mfma_f32_32x32x16_bf16 v[18:33], v[164:167], v[86:89], v[18:33]
	v_mfma_f32_32x32x16_bf16 v[2:17], v[198:201], v[86:89], v[2:17]
	v_lshlrev_b32_e32 v86, 16, v82
	v_and_b32_e32 v87, 0xffff0000, v82
	v_lshlrev_b32_e32 v88, 16, v83
	v_and_b32_e32 v89, 0xffff0000, v83
	v_lshlrev_b32_e32 v82, 16, v84
	v_and_b32_e32 v83, 0xffff0000, v84
	v_lshlrev_b32_e32 v84, 16, v85
	v_and_b32_e32 v85, 0xffff0000, v85
	v_pk_mul_f32 v[150:151], v[216:217], v[88:89]
	v_pk_mul_f32 v[152:153], v[214:215], v[86:87]
	v_pk_mul_f32 v[154:155], v[222:223], v[82:83]
	v_pk_mul_f32 v[158:159], v[224:225], v[84:85]
	v_cvt_pk_bf16_f32 v84, v154, v155
	v_cvt_pk_bf16_f32 v82, v152, v153
	v_cvt_pk_bf16_f32 v85, v158, v159
	v_cvt_pk_bf16_f32 v83, v150, v151
	v_pk_fma_f32 v[88:89], v[216:217], v[88:89], v[158:159]
	v_pk_fma_f32 v[86:87], v[214:215], v[86:87], v[154:155]
	s_mov_b64 s[2:3], 0x3000
	v_mfma_f32_32x32x16_bf16 v[50:65], v[110:113], v[82:85], v[50:65]
	v_add_f32_e64 v86, v90, v86
	v_add_f32_e64 v87, v91, v87
	v_add_f32_e64 v88, v92, v88
	v_add_f32_e64 v89, v93, v89
	s_waitcnt vmcnt(5)
	v_pk_mov_b32 v[90:91], v[86:87], v[88:89] op_sel:[1,0]
	v_mov_b32_e32 v87, v89
	v_pk_add_f32 v[86:87], v[90:91], v[86:87]
	v_lshrrev_b32_e32 v161, 3, v191
	v_mfma_f32_32x32x16_bf16 v[34:49], v[194:197], v[82:85], v[34:49]
	s_movk_i32 s1, 0x90
	v_or_b32_e32 v152, v1, v174
	v_add_f32_e64 v150, v86, v87
	v_add_f32_e64 v151, v87, v86
	v_mad_u32_u24 v155, v161, s1, v152
	v_mul_u32_u24_e32 v147, 0x90, v188
	v_mad_u32_u24 v149, v192, s0, v147
	v_and_b32_e32 v147, 32, v0
	v_mfma_f32_32x32x16_bf16 v[18:33], v[206:209], v[82:85], v[18:33]
	v_add_u32_e32 v151, v149, v147
	v_lshrrev_b32_e32 v147, 1, v191
	v_and_b32_e32 v154, 16, v147
	v_add_u32_e32 v160, v149, v154
	v_sub_u32_e32 v147, v189, v154
	s_mov_b64 s[8:9], 0x16000
	s_brev_b32 s0, 60
	v_mfma_f32_32x32x16_bf16 v[2:17], v[210:213], v[82:85], v[2:17]
	v_lshl_add_u64 v[82:83], v[184:185], 0, s[2:3]
	s_mov_b64 s[2:3], 0x3400
	global_load_dwordx4 v[110:113], v[82:83], off
	v_lshl_add_u64 v[82:83], v[184:185], 0, s[2:3]
	s_mov_b64 s[2:3], 0x3800
	global_load_dwordx4 v[90:93], v[82:83], off
	v_lshl_add_u64 v[82:83], v[184:185], 0, s[2:3]
	s_mov_b64 s[2:3], 0x3c00
	global_load_dwordx4 v[86:89], v[82:83], off
	v_lshl_add_u64 v[82:83], v[184:185], 0, s[2:3]
	global_load_dwordx4 v[82:85], v[82:83], off
	s_waitcnt lgkmcnt(0)
	s_barrier
	ds_write_b128 v155, v[142:145] offset:61440
	v_mov_b32_e32 v142, 0x480
	v_mad_u32_u24 v165, v161, s1, v142
	v_add_u32_e32 v157, v152, v165
	ds_write_b128 v157, v[134:137] offset:61440
	v_mov_b32_e32 v134, 0x900
	v_mad_u32_u24 v164, v161, s1, v134
	v_add_u32_e32 v171, v152, v164
	ds_write_b128 v171, v[130:133] offset:61440
	v_mov_b32_e32 v130, 0xd80
	v_mad_u32_u24 v163, v161, s1, v130
	v_add_u32_e32 v174, v152, v163
	ds_write_b128 v174, v[138:141] offset:61440
	ds_read_b128 v[142:145], v151 offset:61440
	ds_read_b128 v[138:141], v151 offset:61456
	ds_read_b128 v[134:137], v151 offset:61504
	ds_read_b128 v[130:133], v151 offset:61520
	ds_read_b128 v[166:169], v160 offset:61440
	ds_read_b128 v[192:195], v160 offset:61472
	ds_read_b128 v[196:199], v147 offset:58368
	ds_read_b128 v[200:203], v147 offset:58400
	ds_read_b128 v[204:207], v160 offset:61504
	ds_read_b128 v[208:211], v160 offset:61536
	ds_read_b128 v[212:215], v147 offset:58432
	ds_read_b128 v[216:219], v147 offset:58464
	s_waitcnt lgkmcnt(0)
	v_pk_add_f32 v[152:153], v[168:169], v[198:199]
	v_pk_add_f32 v[158:159], v[166:167], v[196:197]
	v_pk_add_f32 v[166:167], v[194:195], v[202:203]
	v_pk_add_f32 v[168:169], v[192:193], v[200:201]
	v_pk_add_f32 v[192:193], v[210:211], v[218:219]
	v_pk_add_f32 v[194:195], v[208:209], v[216:217]
	v_pk_add_f32 v[172:173], v[206:207], v[214:215]
	v_pk_add_f32 v[184:185], v[204:205], v[212:213]
	v_pk_add_f32 v[62:63], v[194:195], v[62:63]
	v_pk_add_f32 v[54:55], v[168:169], v[54:55]
	v_pk_add_f32 v[64:65], v[192:193], v[64:65]
	v_pk_add_f32 v[56:57], v[166:167], v[56:57]
	ds_write_b128 v155, v[114:117] offset:61440
	ds_write_b128 v157, v[118:121] offset:61440
	ds_write_b128 v171, v[122:125] offset:61440
	ds_write_b128 v174, v[126:129] offset:61440
	ds_read_b128 v[126:129], v151 offset:61440
	ds_read_b128 v[122:125], v151 offset:61456
	ds_read_b128 v[118:121], v151 offset:61504
	ds_read_b128 v[114:117], v151 offset:61520
	ds_read_b128 v[166:169], v160 offset:61440
	ds_read_b128 v[192:195], v160 offset:61472
	ds_read_b128 v[196:199], v147 offset:58496
	ds_read_b128 v[200:203], v147 offset:58528
	ds_read_b128 v[204:207], v160 offset:61504
	ds_read_b128 v[208:211], v160 offset:61536
	ds_read_b128 v[212:215], v147 offset:58560
	ds_read_b128 v[216:219], v147 offset:58592
	v_pk_add_f32 v[52:53], v[152:153], v[52:53]
	v_pk_add_f32 v[50:51], v[158:159], v[50:51]
	s_waitcnt lgkmcnt(0)
	v_pk_add_f32 v[152:153], v[168:169], v[198:199]
	v_pk_add_f32 v[158:159], v[166:167], v[196:197]
	v_pk_add_f32 v[166:167], v[194:195], v[202:203]
	v_pk_add_f32 v[168:169], v[192:193], v[200:201]
	v_pk_add_f32 v[192:193], v[210:211], v[218:219]
	v_pk_add_f32 v[194:195], v[208:209], v[216:217]
	v_pk_add_f32 v[58:59], v[184:185], v[58:59]
	v_pk_add_f32 v[60:61], v[172:173], v[60:61]
	v_pk_add_f32 v[172:173], v[206:207], v[214:215]
	v_pk_add_f32 v[184:185], v[204:205], v[212:213]
	v_pk_add_f32 v[46:47], v[194:195], v[46:47]
	v_pk_add_f32 v[38:39], v[168:169], v[38:39]
	v_pk_add_f32 v[48:49], v[192:193], v[48:49]
	v_pk_add_f32 v[40:41], v[166:167], v[40:41]
	ds_write_b128 v155, v[102:105] offset:61440
	ds_write_b128 v157, v[94:97] offset:61440
	ds_write_b128 v171, v[98:101] offset:61440
	ds_write_b128 v174, v[106:109] offset:61440
	ds_read_b128 v[106:109], v151 offset:61440
	ds_read_b128 v[102:105], v151 offset:61456
	ds_read_b128 v[98:101], v151 offset:61504
	ds_read_b128 v[94:97], v151 offset:61520
	ds_read_b128 v[166:169], v160 offset:61440
	ds_read_b128 v[192:195], v160 offset:61472
	ds_read_b128 v[196:199], v147 offset:58624
	ds_read_b128 v[200:203], v147 offset:58656
	ds_read_b128 v[204:207], v160 offset:61504
	ds_read_b128 v[208:211], v160 offset:61536
	ds_read_b128 v[212:215], v147 offset:58688
	ds_read_b128 v[216:219], v147 offset:58720
	v_pk_add_f32 v[36:37], v[152:153], v[36:37]
	v_pk_add_f32 v[34:35], v[158:159], v[34:35]
	s_waitcnt lgkmcnt(0)
	v_pk_add_f32 v[152:153], v[168:169], v[198:199]
	v_pk_add_f32 v[158:159], v[166:167], v[196:197]
	v_pk_add_f32 v[166:167], v[194:195], v[202:203]
	v_pk_add_f32 v[168:169], v[192:193], v[200:201]
	v_pk_add_f32 v[192:193], v[210:211], v[218:219]
	v_pk_add_f32 v[194:195], v[208:209], v[216:217]
	v_add_f32_e32 v149, 0, v142
	v_pk_add_f32 v[42:43], v[184:185], v[42:43]
	v_pk_add_f32 v[44:45], v[172:173], v[44:45]
	v_pk_add_f32 v[172:173], v[206:207], v[214:215]
	v_pk_add_f32 v[184:185], v[204:205], v[212:213]
	v_pk_add_f32 v[30:31], v[194:195], v[30:31]
	v_pk_add_f32 v[22:23], v[168:169], v[22:23]
	v_pk_add_f32 v[32:33], v[192:193], v[32:33]
	v_pk_add_f32 v[24:25], v[166:167], v[24:25]
	ds_write_b128 v155, v[66:69] offset:61440
	ds_write_b128 v157, v[70:73] offset:61440
	ds_write_b128 v171, v[74:77] offset:61440
	ds_write_b128 v174, v[78:81] offset:61440
	ds_read_b128 v[78:81], v151 offset:61440
	ds_read_b128 v[74:77], v151 offset:61456
	ds_read_b128 v[70:73], v151 offset:61504
	ds_read_b128 v[66:69], v151 offset:61520
	ds_read_b128 v[166:169], v160 offset:61440
	ds_read_b128 v[192:195], v160 offset:61472
	ds_read_b128 v[196:199], v147 offset:58752
	ds_read_b128 v[200:203], v147 offset:58784
	ds_read_b128 v[204:207], v160 offset:61504
	ds_read_b128 v[208:211], v160 offset:61536
	ds_read_b128 v[212:215], v147 offset:58816
	ds_read_b128 v[216:219], v147 offset:58848
	v_add_f32_e32 v149, v149, v143
	v_mul_f32_e32 v151, v143, v143
	v_fmac_f32_e32 v151, v142, v142
	v_add_f32_e32 v149, v149, v144
	v_fmac_f32_e32 v151, v144, v144
	v_add_f32_e32 v149, v149, v145
	v_fmac_f32_e32 v151, v145, v145
	v_add_f32_e32 v149, v149, v138
	v_fmac_f32_e32 v151, v138, v138
	v_add_f32_e32 v149, v149, v139
	v_fmac_f32_e32 v151, v139, v139
	v_add_f32_e32 v149, v149, v140
	v_fmac_f32_e32 v151, v140, v140
	v_add_f32_e32 v149, v149, v141
	v_fmac_f32_e32 v151, v141, v141
	v_add_f32_e32 v149, v149, v134
	v_fmac_f32_e32 v151, v134, v134
	v_add_f32_e32 v149, v149, v135
	v_fmac_f32_e32 v151, v135, v135
	v_add_f32_e32 v149, v149, v136
	v_fmac_f32_e32 v151, v136, v136
	v_add_f32_e32 v149, v149, v137
	v_fmac_f32_e32 v151, v137, v137
	v_add_f32_e32 v149, v149, v130
	v_fmac_f32_e32 v151, v130, v130
	v_add_f32_e32 v149, v149, v131
	v_fmac_f32_e32 v151, v131, v131
	v_add_f32_e32 v149, v149, v132
	v_fmac_f32_e32 v151, v132, v132
	v_add_f32_e32 v149, v149, v133
	v_fmac_f32_e32 v151, v133, v133
	v_add_f32_e32 v149, v149, v126
	v_fmac_f32_e32 v151, v126, v126
	v_add_f32_e32 v149, v149, v127
	v_fmac_f32_e32 v151, v127, v127
	v_add_f32_e32 v149, v149, v128
	v_fmac_f32_e32 v151, v128, v128
	v_add_f32_e32 v149, v149, v129
	v_fmac_f32_e32 v151, v129, v129
	v_add_f32_e32 v149, v149, v122
	v_fmac_f32_e32 v151, v122, v122
	v_add_f32_e32 v149, v149, v123
	v_fmac_f32_e32 v151, v123, v123
	v_add_f32_e32 v149, v149, v124
	v_fmac_f32_e32 v151, v124, v124
	v_add_f32_e32 v149, v149, v125
	v_fmac_f32_e32 v151, v125, v125
	v_add_f32_e32 v149, v149, v118
	v_fmac_f32_e32 v151, v118, v118
	v_add_f32_e32 v149, v149, v119
	v_fmac_f32_e32 v151, v119, v119
	v_add_f32_e32 v149, v149, v120
	v_fmac_f32_e32 v151, v120, v120
	v_add_f32_e32 v149, v149, v121
	v_fmac_f32_e32 v151, v121, v121
	v_add_f32_e32 v149, v149, v114
	v_fmac_f32_e32 v151, v114, v114
	v_add_f32_e32 v149, v149, v115
	v_fmac_f32_e32 v151, v115, v115
	v_add_f32_e32 v149, v149, v116
	v_fmac_f32_e32 v151, v116, v116
	v_add_f32_e32 v149, v149, v117
	v_fmac_f32_e32 v151, v117, v117
	v_add_f32_e32 v149, v149, v106
	v_fmac_f32_e32 v151, v106, v106
	v_add_f32_e32 v149, v149, v107
	v_fmac_f32_e32 v151, v107, v107
	v_add_f32_e32 v149, v149, v108
	v_fmac_f32_e32 v151, v108, v108
	v_add_f32_e32 v149, v149, v109
	v_fmac_f32_e32 v151, v109, v109
	v_add_f32_e32 v149, v149, v102
	v_fmac_f32_e32 v151, v102, v102
	v_add_f32_e32 v149, v149, v103
	v_fmac_f32_e32 v151, v103, v103
	v_add_f32_e32 v149, v149, v104
	v_fmac_f32_e32 v151, v104, v104
	v_add_f32_e32 v149, v149, v105
	v_fmac_f32_e32 v151, v105, v105
	v_add_f32_e32 v149, v149, v98
	v_fmac_f32_e32 v151, v98, v98
	v_add_f32_e32 v149, v149, v99
	v_fmac_f32_e32 v151, v99, v99
	v_add_f32_e32 v149, v149, v100
	v_fmac_f32_e32 v151, v100, v100
	v_add_f32_e32 v149, v149, v101
	v_fmac_f32_e32 v151, v101, v101
	v_add_f32_e32 v149, v149, v94
	v_fmac_f32_e32 v151, v94, v94
	v_add_f32_e32 v149, v149, v95
	v_fmac_f32_e32 v151, v95, v95
	v_add_f32_e32 v149, v149, v96
	v_fmac_f32_e32 v151, v96, v96
	v_add_f32_e32 v149, v149, v97
	v_fmac_f32_e32 v151, v97, v97
	s_waitcnt lgkmcnt(0)
	v_add_f32_e32 v149, v149, v78
	v_fmac_f32_e32 v151, v78, v78
	v_add_f32_e32 v149, v149, v79
	v_fmac_f32_e32 v151, v79, v79
	v_add_f32_e32 v149, v149, v80
	v_fmac_f32_e32 v151, v80, v80
	v_add_f32_e32 v149, v149, v81
	v_fmac_f32_e32 v151, v81, v81
	v_add_f32_e32 v149, v149, v74
	v_fmac_f32_e32 v151, v74, v74
	v_add_f32_e32 v149, v149, v75
	v_fmac_f32_e32 v151, v75, v75
	v_add_f32_e32 v149, v149, v76
	v_pk_add_f32 v[20:21], v[152:153], v[20:21]
	v_pk_add_f32 v[152:153], v[168:169], v[198:199]
	v_pk_add_f32 v[168:169], v[192:193], v[200:201]
	v_fmac_f32_e32 v151, v76, v76
	v_add_f32_e32 v149, v149, v77
	v_pk_add_f32 v[6:7], v[168:169], v[6:7]
	v_fmac_f32_e32 v151, v77, v77
	v_add_f32_e32 v149, v149, v70
	v_pk_mul_f32 v[168:169], v[70:71], v[70:71]
	v_pk_add_f32 v[18:19], v[158:159], v[18:19]
	v_pk_add_f32 v[158:159], v[166:167], v[196:197]
	v_pk_add_f32 v[166:167], v[194:195], v[202:203]
	v_add_f32_e32 v149, v149, v71
	v_add_f32_e32 v151, v151, v168
	v_pk_add_f32 v[8:9], v[166:167], v[8:9]
	v_pk_mul_f32 v[166:167], v[72:73], v[72:73]
	v_add_f32_e32 v151, v151, v169
	v_add_f32_e32 v149, v149, v72
	v_add_f32_e32 v149, v149, v73
	v_add_f32_e32 v151, v151, v166
	v_add_f32_e32 v151, v151, v167
	v_add_f32_e32 v149, v149, v66
	v_pk_mul_f32 v[168:169], v[66:67], v[66:67]
	v_add_f32_e32 v149, v149, v67
	v_add_f32_e32 v151, v151, v168
	v_pk_mul_f32 v[166:167], v[68:69], v[68:69]
	v_add_f32_e32 v151, v151, v169
	v_add_f32_e32 v149, v149, v68
	v_add_f32_e32 v169, v149, v69
	v_add_f32_e32 v149, v151, v166
	v_add_f32_e32 v168, v149, v167
	v_mov_b32_e32 v167, v169
	v_mov_b32_e32 v166, v168
	s_nop 0
	v_permlane32_swap_b32_e32 v169, v167
	v_permlane32_swap_b32_e32 v168, v166
	v_readfirstlane_b32 s3, v187
	v_pk_add_f32 v[166:167], v[168:169], v[166:167]
	v_lshl_add_u64 v[168:169], v[180:181], 0, s[8:9]
	s_mov_b32 m0, s3
	s_nop 0
	global_load_lds_dwordx4 v[168:169], off
	global_load_lds_dwordx4 v[168:169], off offset:1024
	global_load_lds_dwordx4 v[168:169], off offset:2048
	global_load_lds_dwordx4 v[168:169], off offset:3072
	v_pk_mul_f32 v[166:167], v[166:167], s[0:1] op_sel_hi:[1,0]
	s_mov_b32 s2, 0x800000
	v_fma_f32 v149, -v167, v167, v166
	v_add_f32_e32 v149, 0x3727c5ac, v149
	v_mul_f32_e32 v151, 0x4b800000, v149
	v_cmp_gt_f32_e32 vcc, s2, v149
	v_pk_add_f32 v[4:5], v[152:153], v[4:5]
	v_pk_add_f32 v[2:3], v[158:159], v[2:3]
	v_cndmask_b32_e32 v149, v149, v151, vcc
	v_rsq_f32_e32 v149, v149
	v_pk_add_f32 v[26:27], v[184:185], v[26:27]
	v_pk_add_f32 v[28:29], v[172:173], v[28:29]
	v_pk_add_f32 v[172:173], v[206:207], v[214:215]
	v_mul_f32_e32 v151, 0x45800000, v149
	v_cndmask_b32_e32 v152, v149, v151, vcc
	v_mul_f32_e64 v158, v152, -v167
	v_pk_add_f32 v[184:185], v[204:205], v[212:213]
	v_pk_add_f32 v[192:193], v[210:211], v[218:219]
	v_pk_add_f32 v[194:195], v[208:209], v[216:217]
	v_pk_fma_f32 v[142:143], v[152:153], v[142:143], v[158:159] op_sel_hi:[0,1,0]
	v_pk_fma_f32 v[144:145], v[152:153], v[144:145], v[158:159] op_sel_hi:[0,1,0]
	v_pk_fma_f32 v[138:139], v[152:153], v[138:139], v[158:159] op_sel_hi:[0,1,0]
	v_pk_fma_f32 v[140:141], v[152:153], v[140:141], v[158:159] op_sel_hi:[0,1,0]
	v_pk_fma_f32 v[134:135], v[152:153], v[134:135], v[158:159] op_sel_hi:[0,1,0]
	v_pk_fma_f32 v[136:137], v[152:153], v[136:137], v[158:159] op_sel_hi:[0,1,0]
	v_pk_fma_f32 v[130:131], v[152:153], v[130:131], v[158:159] op_sel_hi:[0,1,0]
	v_pk_fma_f32 v[132:133], v[152:153], v[132:133], v[158:159] op_sel_hi:[0,1,0]
	v_pk_fma_f32 v[126:127], v[152:153], v[126:127], v[158:159] op_sel_hi:[0,1,0]
	v_pk_fma_f32 v[128:129], v[152:153], v[128:129], v[158:159] op_sel_hi:[0,1,0]
	v_pk_fma_f32 v[122:123], v[152:153], v[122:123], v[158:159] op_sel_hi:[0,1,0]
	v_pk_fma_f32 v[124:125], v[152:153], v[124:125], v[158:159] op_sel_hi:[0,1,0]
	v_pk_fma_f32 v[118:119], v[152:153], v[118:119], v[158:159] op_sel_hi:[0,1,0]
	v_pk_fma_f32 v[120:121], v[152:153], v[120:121], v[158:159] op_sel_hi:[0,1,0]
	v_pk_fma_f32 v[114:115], v[152:153], v[114:115], v[158:159] op_sel_hi:[0,1,0]
	v_pk_fma_f32 v[116:117], v[152:153], v[116:117], v[158:159] op_sel_hi:[0,1,0]
	v_pk_fma_f32 v[106:107], v[152:153], v[106:107], v[158:159] op_sel_hi:[0,1,0]
	v_pk_fma_f32 v[108:109], v[152:153], v[108:109], v[158:159] op_sel_hi:[0,1,0]
	v_pk_fma_f32 v[102:103], v[152:153], v[102:103], v[158:159] op_sel_hi:[0,1,0]
	v_pk_fma_f32 v[104:105], v[152:153], v[104:105], v[158:159] op_sel_hi:[0,1,0]
	v_pk_fma_f32 v[98:99], v[152:153], v[98:99], v[158:159] op_sel_hi:[0,1,0]
	v_pk_fma_f32 v[100:101], v[152:153], v[100:101], v[158:159] op_sel_hi:[0,1,0]
	v_pk_fma_f32 v[94:95], v[152:153], v[94:95], v[158:159] op_sel_hi:[0,1,0]
	v_pk_fma_f32 v[96:97], v[152:153], v[96:97], v[158:159] op_sel_hi:[0,1,0]
	v_pk_fma_f32 v[78:79], v[152:153], v[78:79], v[158:159] op_sel_hi:[0,1,0]
	v_pk_fma_f32 v[80:81], v[152:153], v[80:81], v[158:159] op_sel_hi:[0,1,0]
	v_pk_fma_f32 v[74:75], v[152:153], v[74:75], v[158:159] op_sel_hi:[0,1,0]
	v_pk_fma_f32 v[76:77], v[152:153], v[76:77], v[158:159] op_sel_hi:[0,1,0]
	v_pk_add_f32 v[14:15], v[194:195], v[14:15]
	v_pk_add_f32 v[10:11], v[184:185], v[10:11]
	v_pk_add_f32 v[16:17], v[192:193], v[16:17]
	v_pk_add_f32 v[12:13], v[172:173], v[12:13]
	v_cvt_pk_bf16_f32 v141, v140, v141
	v_cvt_pk_bf16_f32 v140, v138, v139
	v_cvt_pk_bf16_f32 v139, v144, v145
	v_cvt_pk_bf16_f32 v138, v142, v143
	v_cvt_pk_bf16_f32 v133, v132, v133
	v_cvt_pk_bf16_f32 v132, v130, v131
	v_cvt_pk_bf16_f32 v131, v136, v137
	v_cvt_pk_bf16_f32 v130, v134, v135
	v_cvt_pk_bf16_f32 v125, v124, v125
	v_cvt_pk_bf16_f32 v124, v122, v123
	v_cvt_pk_bf16_f32 v123, v128, v129
	v_cvt_pk_bf16_f32 v122, v126, v127
	v_cvt_pk_bf16_f32 v117, v116, v117
	v_cvt_pk_bf16_f32 v116, v114, v115
	v_cvt_pk_bf16_f32 v115, v120, v121
	v_cvt_pk_bf16_f32 v114, v118, v119
	v_cvt_pk_bf16_f32 v105, v104, v105
	v_cvt_pk_bf16_f32 v104, v102, v103
	v_cvt_pk_bf16_f32 v103, v108, v109
	v_cvt_pk_bf16_f32 v102, v106, v107
	v_cvt_pk_bf16_f32 v109, v96, v97
	v_cvt_pk_bf16_f32 v108, v94, v95
	v_cvt_pk_bf16_f32 v107, v100, v101
	v_cvt_pk_bf16_f32 v106, v98, v99
	v_cvt_pk_bf16_f32 v121, v76, v77
	v_cvt_pk_bf16_f32 v120, v74, v75
	v_cvt_pk_bf16_f32 v119, v80, v81
	v_cvt_pk_bf16_f32 v118, v78, v79
	v_pk_fma_f32 v[172:173], v[152:153], v[70:71], v[158:159] op_sel_hi:[0,1,0]
	v_pk_fma_f32 v[94:95], v[152:153], v[72:73], v[158:159] op_sel_hi:[0,1,0]
	v_pk_fma_f32 v[184:185], v[152:153], v[66:67], v[158:159] op_sel_hi:[0,1,0]
	v_pk_fma_f32 v[96:97], v[152:153], v[68:69], v[158:159] op_sel_hi:[0,1,0]
	ds_read_b128 v[66:69], v176
	ds_read_b128 v[70:73], v176 offset:1024
	ds_read_b128 v[74:77], v176 offset:2048
	ds_read_b128 v[78:81], v176 offset:3072
	ds_read_b128 v[98:101], v176 offset:4096
	ds_read_b128 v[126:129], v176 offset:5120
	ds_read_b128 v[134:137], v176 offset:6144
	ds_read_b128 v[142:145], v176 offset:7168
	ds_read_b128 v[166:169], v176 offset:8192
	ds_read_b128 v[192:195], v176 offset:9216
	v_cvt_pk_bf16_f32 v97, v96, v97
	v_cvt_pk_bf16_f32 v96, v184, v185
	v_cvt_pk_bf16_f32 v95, v94, v95
	v_cvt_pk_bf16_f32 v94, v172, v173
	ds_read_b128 v[196:199], v176 offset:10240
	ds_read_b128 v[200:203], v176 offset:11264
	ds_read_b128 v[204:207], v176 offset:12288
	ds_read_b128 v[208:211], v176 offset:13312
	ds_read_b128 v[212:215], v176 offset:14336
	s_waitcnt lgkmcnt(0)
	v_mfma_f32_32x32x16_bf16 v[50:65], v[66:69], v[138:141], v[50:65]
	v_mfma_f32_32x32x16_bf16 v[34:49], v[70:73], v[138:141], v[34:49]
	v_mfma_f32_32x32x16_bf16 v[18:33], v[74:77], v[138:141], v[18:33]
	v_mfma_f32_32x32x16_bf16 v[2:17], v[78:81], v[138:141], v[2:17]
	v_mfma_f32_32x32x16_bf16 v[66:81], v[98:101], v[138:141], 0
	v_mfma_f32_32x32x16_bf16 v[50:65], v[126:129], v[130:133], v[50:65]
	v_mfma_f32_32x32x16_bf16 v[34:49], v[134:137], v[130:133], v[34:49]
	v_mfma_f32_32x32x16_bf16 v[18:33], v[142:145], v[130:133], v[18:33]
	ds_read_b128 v[98:101], v176 offset:15360
	ds_read_b128 v[126:129], v176 offset:16384
	ds_read_b128 v[134:137], v176 offset:17408
	ds_read_b128 v[138:141], v176 offset:18432
	ds_read_b128 v[142:145], v176 offset:19456
	v_mfma_f32_32x32x16_bf16 v[2:17], v[166:169], v[130:133], v[2:17]
	v_mfma_f32_32x32x16_bf16 v[66:81], v[192:195], v[130:133], v[66:81]
	v_mfma_f32_32x32x16_bf16 v[50:65], v[196:199], v[122:125], v[50:65]
	v_mfma_f32_32x32x16_bf16 v[34:49], v[200:203], v[122:125], v[34:49]
	v_mfma_f32_32x32x16_bf16 v[18:33], v[204:207], v[122:125], v[18:33]
	v_mfma_f32_32x32x16_bf16 v[2:17], v[208:211], v[122:125], v[2:17]
	v_mfma_f32_32x32x16_bf16 v[66:81], v[212:215], v[122:125], v[66:81]
	s_mov_b64 s[8:9], 0x1a000
	v_readfirstlane_b32 s3, v186
	s_waitcnt lgkmcnt(0)
	v_mfma_f32_32x32x16_bf16 v[50:65], v[98:101], v[114:117], v[50:65]
	v_lshl_add_u64 v[98:99], v[180:181], 0, s[8:9]
	s_mov_b32 m0, s3
	s_waitcnt vmcnt(8) lgkmcnt(0)
	s_barrier
	global_load_lds_dwordx4 v[98:99], off
	global_load_lds_dwordx4 v[98:99], off offset:1024
	global_load_lds_dwordx4 v[98:99], off offset:2048
	global_load_lds_dwordx4 v[98:99], off offset:3072
	v_mfma_f32_32x32x16_bf16 v[34:49], v[126:129], v[114:117], v[34:49]
	ds_read_b128 v[98:101], v176 offset:20480
	ds_read_b128 v[122:125], v176 offset:21504
	v_mfma_f32_32x32x16_bf16 v[18:33], v[134:137], v[114:117], v[18:33]
	v_mfma_f32_32x32x16_bf16 v[2:17], v[138:141], v[114:117], v[2:17]
	ds_read_b128 v[126:129], v176 offset:22528
	ds_read_b128 v[130:133], v176 offset:23552
	ds_read_b128 v[134:137], v176 offset:24576
	ds_read_b128 v[138:141], v176 offset:25600
	ds_read_b128 v[166:169], v176 offset:26624
	ds_read_b128 v[192:195], v176 offset:27648
	ds_read_b128 v[196:199], v176 offset:28672
	ds_read_b128 v[200:203], v176 offset:29696
	v_mfma_f32_32x32x16_bf16 v[66:81], v[142:145], v[114:117], v[66:81]
	s_waitcnt lgkmcnt(0)
	v_mfma_f32_32x32x16_bf16 v[34:49], v[122:125], v[102:105], v[34:49]
	v_mfma_f32_32x32x16_bf16 v[18:33], v[126:129], v[102:105], v[18:33]
	v_mfma_f32_32x32x16_bf16 v[2:17], v[130:133], v[102:105], v[2:17]
	ds_read_b128 v[114:117], v176 offset:31744
	ds_read_b128 v[122:125], v176 offset:32768
	ds_read_b128 v[126:129], v176 offset:33792
	ds_read_b128 v[130:133], v176 offset:30720
	ds_read_b128 v[142:145], v176 offset:34816
	v_mfma_f32_32x32x16_bf16 v[50:65], v[98:101], v[102:105], v[50:65]
	v_mfma_f32_32x32x16_bf16 v[66:81], v[134:137], v[102:105], v[66:81]
	v_mfma_f32_32x32x16_bf16 v[50:65], v[138:141], v[106:109], v[50:65]
	v_mfma_f32_32x32x16_bf16 v[34:49], v[166:169], v[106:109], v[34:49]
	ds_read_b128 v[102:105], v176 offset:35840
	ds_read_b128 v[134:137], v176 offset:36864
	ds_read_b128 v[138:141], v176 offset:37888
	ds_read_b128 v[166:169], v176 offset:38912
	ds_read_b128 v[98:101], v176 offset:39936
	v_mfma_f32_32x32x16_bf16 v[18:33], v[192:195], v[106:109], v[18:33]
	v_mfma_f32_32x32x16_bf16 v[2:17], v[196:199], v[106:109], v[2:17]
	v_mfma_f32_32x32x16_bf16 v[66:81], v[200:203], v[106:109], v[66:81]
	s_waitcnt lgkmcnt(0)
	v_mfma_f32_32x32x16_bf16 v[50:65], v[130:133], v[118:121], v[50:65]
	v_mfma_f32_32x32x16_bf16 v[34:49], v[114:117], v[118:121], v[34:49]
	v_mfma_f32_32x32x16_bf16 v[18:33], v[122:125], v[118:121], v[18:33]
	v_mfma_f32_32x32x16_bf16 v[2:17], v[126:129], v[118:121], v[2:17]
	v_mfma_f32_32x32x16_bf16 v[66:81], v[142:145], v[118:121], v[66:81]
	s_mov_b64 s[8:9], 0x1e000
	v_readfirstlane_b32 s3, v190
	v_mfma_f32_32x32x16_bf16 v[50:65], v[102:105], v[94:97], v[50:65]
	v_lshl_add_u64 v[102:103], v[180:181], 0, s[8:9]
	s_mov_b32 m0, s3
	s_waitcnt vmcnt(4) lgkmcnt(0)
	s_barrier
	global_load_lds_dwordx4 v[102:103], off
	global_load_lds_dwordx4 v[102:103], off offset:1024
	global_load_lds_dwordx4 v[102:103], off offset:2048
	global_load_lds_dwordx4 v[102:103], off offset:3072
	s_waitcnt vmcnt(4)
	v_mfma_f32_32x32x16_bf16 v[34:49], v[134:137], v[94:97], v[34:49]
	ds_read_b128 v[102:105], v176 offset:40960
	ds_read_b128 v[106:109], v176 offset:41984
	v_mfma_f32_32x32x16_bf16 v[18:33], v[138:141], v[94:97], v[18:33]
	ds_read_b128 v[114:117], v176 offset:43008
	ds_read_b128 v[118:121], v176 offset:44032
	ds_read_b128 v[122:125], v189 offset:58112
	ds_read_b128 v[126:129], v189 offset:58128
	ds_read_b128 v[130:133], v176 offset:45056
	ds_read_b128 v[134:137], v176 offset:46080
	ds_read_b128 v[138:141], v176 offset:47104
	ds_read_b128 v[142:145], v176 offset:48128
	ds_read_b128 v[190:193], v189 offset:58176
	ds_read_b128 v[194:197], v189 offset:58192
	v_mfma_f32_32x32x16_bf16 v[2:17], v[166:169], v[94:97], v[2:17]
	v_lshlrev_b32_e32 v152, 16, v110
	v_and_b32_e32 v153, 0xffff0000, v110
	v_lshlrev_b32_e32 v158, 16, v111
	v_and_b32_e32 v159, 0xffff0000, v111
	v_lshlrev_b32_e32 v110, 16, v112
	v_and_b32_e32 v111, 0xffff0000, v112
	v_lshlrev_b32_e32 v112, 16, v113
	v_and_b32_e32 v113, 0xffff0000, v113
	s_waitcnt lgkmcnt(0)
	v_pk_mul_f32 v[166:167], v[122:123], v[152:153]
	v_pk_mul_f32 v[168:169], v[124:125], v[158:159]
	v_pk_mul_f32 v[128:129], v[128:129], v[112:113]
	v_pk_mul_f32 v[126:127], v[126:127], v[110:111]
	v_cvt_pk_bf16_f32 v113, v128, v129
	v_cvt_pk_bf16_f32 v112, v126, v127
	v_cvt_pk_bf16_f32 v111, v168, v169
	v_cvt_pk_bf16_f32 v110, v166, v167
	v_pk_fma_f32 v[152:153], v[122:123], v[152:153], v[126:127]
	v_pk_fma_f32 v[158:159], v[124:125], v[158:159], v[128:129]
	v_mfma_f32_32x32x16_bf16 v[50:65], v[102:105], v[110:113], v[50:65]
	v_mfma_f32_32x32x16_bf16 v[34:49], v[106:109], v[110:113], v[34:49]
	v_mfma_f32_32x32x16_bf16 v[18:33], v[114:117], v[110:113], v[18:33]
	ds_read_b128 v[102:105], v176 offset:49152
	ds_read_b128 v[106:109], v176 offset:50176
	ds_read_b128 v[114:117], v176 offset:51200
	ds_read_b128 v[122:125], v176 offset:52224
	ds_read_b128 v[126:129], v189 offset:58240
	ds_read_b128 v[166:169], v189 offset:58256
	v_mfma_f32_32x32x16_bf16 v[2:17], v[118:121], v[110:113], v[2:17]
	v_lshlrev_b32_e32 v110, 16, v90
	v_and_b32_e32 v111, 0xffff0000, v90
	v_lshlrev_b32_e32 v112, 16, v91
	v_and_b32_e32 v113, 0xffff0000, v91
	v_lshlrev_b32_e32 v90, 16, v92
	v_and_b32_e32 v91, 0xffff0000, v92
	v_lshlrev_b32_e32 v92, 16, v93
	v_and_b32_e32 v93, 0xffff0000, v93
	v_pk_mul_f32 v[172:173], v[196:197], v[92:93]
	v_pk_mul_f32 v[184:185], v[194:195], v[90:91]
	v_pk_mul_f32 v[118:119], v[190:191], v[110:111]
	v_pk_mul_f32 v[120:121], v[192:193], v[112:113]
	v_pk_fma_f32 v[110:111], v[190:191], v[110:111], v[184:185]
	v_pk_fma_f32 v[112:113], v[192:193], v[112:113], v[172:173]
	v_pk_add_f32 v[110:111], v[152:153], v[110:111]
	v_pk_add_f32 v[112:113], v[158:159], v[112:113]
	v_cvt_pk_bf16_f32 v90, v118, v119
	v_pk_mov_b32 v[118:119], v[110:111], v[112:113] op_sel:[1,0]
	v_mov_b32_e32 v111, v113
	v_cvt_pk_bf16_f32 v93, v172, v173
	v_cvt_pk_bf16_f32 v92, v184, v185
	v_cvt_pk_bf16_f32 v91, v120, v121
	v_pk_add_f32 v[110:111], v[118:119], v[110:111]
	s_nop 0
	v_mfma_f32_32x32x16_bf16 v[50:65], v[130:133], v[90:93], v[50:65]
	v_add_f32_e64 v152, v110, v111
	v_add_f32_e64 v153, v111, v110
	v_mfma_f32_32x32x16_bf16 v[34:49], v[134:137], v[90:93], v[34:49]
	v_mfma_f32_32x32x16_bf16 v[18:33], v[138:141], v[90:93], v[18:33]
	ds_read_b128 v[110:113], v176 offset:53248
	ds_read_b128 v[118:121], v176 offset:54272
	ds_read_b128 v[130:133], v176 offset:55296
	ds_read_b128 v[134:137], v176 offset:56320
	ds_read_b128 v[138:141], v189 offset:58304
	ds_read_b128 v[190:193], v189 offset:58320
	v_mfma_f32_32x32x16_bf16 v[2:17], v[142:145], v[90:93], v[2:17]
	v_lshlrev_b32_e32 v90, 16, v86
	v_and_b32_e32 v91, 0xffff0000, v86
	v_lshlrev_b32_e32 v92, 16, v87
	v_and_b32_e32 v93, 0xffff0000, v87
	v_lshlrev_b32_e32 v86, 16, v88
	v_and_b32_e32 v87, 0xffff0000, v88
	v_lshlrev_b32_e32 v88, 16, v89
	v_and_b32_e32 v89, 0xffff0000, v89
	s_waitcnt lgkmcnt(0)
	v_pk_mul_f32 v[142:143], v[128:129], v[92:93]
	v_pk_mul_f32 v[144:145], v[126:127], v[90:91]
	v_pk_mul_f32 v[158:159], v[166:167], v[86:87]
	v_pk_mul_f32 v[166:167], v[168:169], v[88:89]
	v_cvt_pk_bf16_f32 v88, v158, v159
	v_cvt_pk_bf16_f32 v86, v144, v145
	v_cvt_pk_bf16_f32 v89, v166, v167
	v_cvt_pk_bf16_f32 v87, v142, v143
	v_pk_fma_f32 v[92:93], v[128:129], v[92:93], v[166:167]
	v_pk_fma_f32 v[90:91], v[126:127], v[90:91], v[158:159]
	v_mfma_f32_32x32x16_bf16 v[50:65], v[102:105], v[86:89], v[50:65]
	v_mfma_f32_32x32x16_bf16 v[34:49], v[106:109], v[86:89], v[34:49]
	v_mfma_f32_32x32x16_bf16 v[18:33], v[114:117], v[86:89], v[18:33]
	v_mfma_f32_32x32x16_bf16 v[2:17], v[122:125], v[86:89], v[2:17]
	v_lshlrev_b32_e32 v86, 16, v82
	v_and_b32_e32 v87, 0xffff0000, v82
	v_lshlrev_b32_e32 v88, 16, v83
	v_and_b32_e32 v89, 0xffff0000, v83
	v_lshlrev_b32_e32 v82, 16, v84
	v_and_b32_e32 v83, 0xffff0000, v84
	v_lshlrev_b32_e32 v84, 16, v85
	v_and_b32_e32 v85, 0xffff0000, v85
	v_mfma_f32_32x32x16_bf16 v[66:81], v[98:101], v[94:97], v[66:81]
	v_mul_f32_e64 v102, v140, v88
	v_mul_f32_e64 v103, v141, v89
	v_mul_f32_e64 v104, v138, v86
	v_mul_f32_e64 v105, v139, v87
	v_mul_f32_e64 v106, v190, v82
	v_mul_f32_e64 v107, v191, v83
	v_pk_mul_f32 v[108:109], v[192:193], v[84:85]
	v_cvt_pk_bf16_f32 v84, v106, v107
	v_cvt_pk_bf16_f32 v82, v104, v105
	v_cvt_pk_bf16_f32 v85, v108, v109
	v_cvt_pk_bf16_f32 v83, v102, v103
	s_waitcnt vmcnt(4) lgkmcnt(0)
	s_nop 0
	v_mfma_f32_32x32x16_bf16 v[50:65], v[110:113], v[82:85], v[50:65]
	s_barrier
	v_permlane32_swap_b32_e32 v162, v150
	v_permlane32_swap_b32_e32 v170, v148
	v_mov_b32_e32 v171, v162
	v_mov_b32_e32 v149, v150
	v_mfma_f32_32x32x16_bf16 v[34:49], v[118:121], v[82:85], v[34:49]
	v_add_f32_e64 v70, v170, v148
	v_add_f32_e64 v71, v171, v149
	s_mov_b32 s8, 0x3e3504f3
	v_add_f32_e64 v66, v66, v70
	v_add_f32_e64 v67, v67, v71
	v_or_b32_e32 v182, v182, v188
	v_mul_f32_e32 v74, v51, v51
	v_fmac_f32_e32 v74, v50, v50
	v_fmac_f32_e32 v74, v52, v52
	v_mfma_f32_32x32x16_bf16 v[18:33], v[130:133], v[82:85], v[18:33]
	v_fmac_f32_e32 v74, v53, v53
	v_fmac_f32_e32 v74, v54, v54
	v_fmac_f32_e32 v74, v55, v55
	v_fmac_f32_e32 v74, v56, v56
	v_fmac_f32_e32 v74, v57, v57
	v_fmac_f32_e32 v74, v58, v58
	v_fmac_f32_e32 v74, v59, v59
	v_mfma_f32_32x32x16_bf16 v[2:17], v[134:137], v[82:85], v[2:17]
	ds_read_b128 v[82:85], v147 offset:59904
	v_fmac_f32_e32 v74, v60, v60
	v_fmac_f32_e32 v74, v61, v61
	v_fmac_f32_e32 v74, v62, v62
	v_fmac_f32_e32 v74, v63, v63
	s_waitcnt lgkmcnt(0)
	v_pk_add_f32 v[66:67], v[82:83], v[66:67]
	v_fmac_f32_e32 v74, v64, v64
	v_pk_mul_f32 v[130:131], v[66:67], s[8:9] op_sel_hi:[1,0]
	v_lshlrev_b64 v[66:67], 5, v[182:183]
	v_lshl_add_u64 v[134:135], s[4:5], 0, v[66:67]
	v_add_f32_e32 v66, 0, v50
	v_add_f32_e32 v66, v66, v51
	v_add_f32_e32 v66, v66, v52
	v_add_f32_e32 v66, v66, v53
	v_add_f32_e32 v66, v66, v54
	v_add_f32_e32 v66, v66, v55
	v_add_f32_e32 v66, v66, v56
	v_add_f32_e32 v66, v66, v57
	v_add_f32_e32 v66, v66, v58
	v_add_f32_e32 v66, v66, v59
	v_add_f32_e32 v66, v66, v60
	v_add_f32_e32 v66, v66, v61
	v_add_f32_e32 v66, v66, v62
	v_add_f32_e32 v66, v66, v63
	v_add_f32_e32 v66, v66, v64
	v_add_f32_e32 v66, v66, v65
	v_fmac_f32_e32 v74, v65, v65
	v_add_f32_e32 v66, v66, v34
	v_fmac_f32_e32 v74, v34, v34
	v_add_f32_e32 v66, v66, v35
	v_fmac_f32_e32 v74, v35, v35
	v_add_f32_e32 v66, v66, v36
	v_fmac_f32_e32 v74, v36, v36
	v_add_f32_e32 v66, v66, v37
	v_fmac_f32_e32 v74, v37, v37
	v_add_f32_e32 v66, v66, v38
	v_fmac_f32_e32 v74, v38, v38
	v_add_f32_e32 v66, v66, v39
	v_fmac_f32_e32 v74, v39, v39
	v_add_f32_e32 v66, v66, v40
	v_fmac_f32_e32 v74, v40, v40
	v_add_f32_e32 v66, v66, v41
	v_fmac_f32_e32 v74, v41, v41
	v_add_f32_e32 v66, v66, v42
	v_fmac_f32_e32 v74, v42, v42
	v_add_f32_e32 v66, v66, v43
	v_fmac_f32_e32 v74, v43, v43
	v_add_f32_e32 v66, v66, v44
	v_fmac_f32_e32 v74, v44, v44
	v_add_f32_e32 v66, v66, v45
	v_fmac_f32_e32 v74, v45, v45
	v_add_f32_e32 v66, v66, v46
	v_fmac_f32_e32 v74, v46, v46
	v_add_f32_e32 v66, v66, v47
	v_fmac_f32_e32 v74, v47, v47
	v_add_f32_e32 v66, v66, v48
	v_fmac_f32_e32 v74, v48, v48
	v_add_f32_e32 v66, v66, v49
	v_fmac_f32_e32 v74, v49, v49
	v_add_f32_e32 v66, v66, v18
	v_fmac_f32_e32 v74, v18, v18
	v_add_f32_e32 v66, v66, v19
	v_fmac_f32_e32 v74, v19, v19
	v_add_f32_e32 v66, v66, v20
	v_fmac_f32_e32 v74, v20, v20
	v_add_f32_e32 v66, v66, v21
	v_fmac_f32_e32 v74, v21, v21
	v_add_f32_e32 v66, v66, v22
	v_fmac_f32_e32 v74, v22, v22
	v_add_f32_e32 v66, v66, v23
	v_fmac_f32_e32 v74, v23, v23
	v_add_f32_e32 v66, v66, v24
	v_fmac_f32_e32 v74, v24, v24
	v_add_f32_e32 v66, v66, v25
	v_fmac_f32_e32 v74, v25, v25
	v_add_f32_e32 v66, v66, v26
	v_fmac_f32_e32 v74, v26, v26
	v_add_f32_e32 v66, v66, v27
	v_fmac_f32_e32 v74, v27, v27
	v_add_f32_e32 v66, v66, v28
	v_fmac_f32_e32 v74, v28, v28
	v_add_f32_e32 v66, v66, v29
	v_fmac_f32_e32 v74, v29, v29
	v_add_f32_e32 v66, v66, v30
	v_fmac_f32_e32 v74, v30, v30
	v_add_f32_e32 v66, v66, v31
	v_fmac_f32_e32 v74, v31, v31
	v_add_f32_e32 v66, v66, v32
	v_fmac_f32_e32 v74, v32, v32
	v_add_f32_e32 v66, v66, v33
	v_fmac_f32_e32 v74, v33, v33
	v_add_f32_e32 v66, v66, v2
	v_fmac_f32_e32 v74, v2, v2
	v_pk_fma_f32 v[88:89], v[140:141], v[88:89], v[108:109]
	v_pk_fma_f32 v[86:87], v[138:139], v[86:87], v[106:107]
	v_add_f32_e32 v66, v66, v3
	v_fmac_f32_e32 v74, v3, v3
	v_pk_add_f32 v[86:87], v[90:91], v[86:87]
	v_pk_add_f32 v[88:89], v[92:93], v[88:89]
	v_add_f32_e32 v66, v66, v4
	v_fmac_f32_e32 v74, v4, v4
	v_pk_mov_b32 v[90:91], v[86:87], v[88:89] op_sel:[1,0]
	v_mov_b32_e32 v87, v89
	v_add_f32_e32 v66, v66, v5
	v_fmac_f32_e32 v74, v5, v5
	v_pk_add_f32 v[86:87], v[90:91], v[86:87]
	v_add_f32_e32 v66, v66, v6
	v_fmac_f32_e32 v74, v6, v6
	v_pk_add_f32 v[86:87], v[86:87], v[86:87] op_sel:[0,1] op_sel_hi:[1,0]
	v_add_f32_e32 v66, v66, v7
	v_fmac_f32_e32 v74, v7, v7
	v_permlane32_swap_b32_e32 v146, v86
	v_add_f32_e32 v66, v66, v8
	v_fmac_f32_e32 v74, v8, v8
	v_permlane32_swap_b32_e32 v156, v152
	v_mov_b32_e32 v157, v146
	v_mov_b32_e32 v153, v86
	v_add_f32_e32 v66, v66, v9
	v_fmac_f32_e32 v74, v9, v9
	v_pk_mul_f32 v[72:73], v[10:11], v[10:11]
	v_pk_add_f32 v[70:71], v[156:157], v[152:153]
	v_add_f32_e32 v66, v66, v10
	v_add_f32_e32 v72, v74, v72
	v_pk_add_f32 v[68:69], v[68:69], v[70:71]
	v_add_f32_e32 v75, v66, v11
	v_pk_mul_f32 v[70:71], v[12:13], v[12:13]
	v_add_f32_e32 v72, v72, v73
	v_pk_add_f32 v[68:69], v[84:85], v[68:69]
	v_add_f32_e32 v73, v75, v12
	v_add_f32_e32 v70, v72, v70
	v_pk_mul_f32 v[132:133], v[68:69], s[8:9] op_sel_hi:[1,0]
	v_pk_mul_f32 v[68:69], v[14:15], v[14:15]
	v_add_f32_e32 v73, v73, v13
	v_add_f32_e32 v70, v70, v71
	v_add_f32_e32 v71, v73, v14
	v_add_f32_e32 v68, v70, v68
	v_pk_mul_f32 v[66:67], v[16:17], v[16:17]
	v_add_f32_e32 v71, v71, v15
	v_add_f32_e32 v68, v68, v69
	v_add_f32_e32 v69, v71, v16
	v_add_f32_e32 v66, v68, v66
	v_add_f32_e32 v69, v69, v17
	v_add_f32_e32 v68, v66, v67
	v_mov_b32_e32 v67, v69
	v_mov_b32_e32 v66, v68
	s_nop 0
	v_permlane32_swap_b32_e32 v69, v67
	v_permlane32_swap_b32_e32 v68, v66
	v_pk_add_f32 v[66:67], v[68:69], v[66:67]
	v_mov_b32_e32 v155, v175
	v_pk_mul_f32 v[136:137], v[66:67], s[0:1] op_sel_hi:[1,0]
	v_readfirstlane_b32 s0, v187
	v_fma_f32 v66, -v137, v137, v136
	v_add_f32_e32 v66, 0x3727c5ac, v66
	v_cmp_gt_f32_e32 vcc, s2, v66
	s_mov_b64 s[2:3], 0x22000
	v_mul_f32_e32 v67, 0x4b800000, v66
	v_lshl_add_u64 v[138:139], v[180:181], 0, s[2:3]
	s_mov_b32 m0, s0
	v_cndmask_b32_e32 v136, v66, v67, vcc
	ds_read_b128 v[114:117], v147 offset:58880
	ds_read_b128 v[118:121], v147 offset:58912
	ds_read_b128 v[122:125], v147 offset:58944
	ds_read_b128 v[126:129], v147 offset:58976
	ds_read_b128 v[98:101], v147 offset:59008
	ds_read_b128 v[102:105], v147 offset:59040
	ds_read_b128 v[106:109], v147 offset:59072
	ds_read_b128 v[110:113], v147 offset:59104
	ds_read_b128 v[82:85], v147 offset:59136
	ds_read_b128 v[86:89], v147 offset:59168
	ds_read_b128 v[90:93], v147 offset:59200
	ds_read_b128 v[94:97], v147 offset:59232
	ds_read_b128 v[66:69], v147 offset:59264
	ds_read_b128 v[70:73], v147 offset:59296
	ds_read_b128 v[74:77], v147 offset:59328
	ds_read_b128 v[78:81], v147 offset:59360
	global_load_lds_dwordx4 v[138:139], off
	global_load_lds_dwordx4 v[138:139], off offset:1024
	global_load_lds_dwordx4 v[138:139], off offset:2048
	global_load_lds_dwordx4 v[138:139], off offset:3072
	v_rsq_f32_e32 v136, v136
	v_lshl_add_u64 v[134:135], v[134:135], 0, v[154:155]
	global_store_dwordx4 v[134:135], v[130:133], off sc1
	s_nop 1
	v_mul_f32_e32 v130, 0x45800000, v136
	v_cndmask_b32_e32 v162, v136, v130, vcc
	v_mul_f32_e64 v166, v162, -v137
	v_pk_fma_f32 v[134:135], v[162:163], v[50:51], v[166:167] op_sel_hi:[0,1,0]
	v_pk_fma_f32 v[130:131], v[162:163], v[52:53], v[166:167] op_sel_hi:[0,1,0]
	v_pk_fma_f32 v[136:137], v[162:163], v[54:55], v[166:167] op_sel_hi:[0,1,0]
	v_pk_fma_f32 v[132:133], v[162:163], v[56:57], v[166:167] op_sel_hi:[0,1,0]
	v_cvt_pk_bf16_f32 v133, v132, v133
	v_cvt_pk_bf16_f32 v132, v136, v137
	v_cvt_pk_bf16_f32 v131, v130, v131
	v_cvt_pk_bf16_f32 v130, v134, v135
	v_pk_fma_f32 v[138:139], v[162:163], v[58:59], v[166:167] op_sel_hi:[0,1,0]
	v_pk_fma_f32 v[134:135], v[162:163], v[60:61], v[166:167] op_sel_hi:[0,1,0]
	v_pk_fma_f32 v[140:141], v[162:163], v[62:63], v[166:167] op_sel_hi:[0,1,0]
	v_pk_fma_f32 v[136:137], v[162:163], v[64:65], v[166:167] op_sel_hi:[0,1,0]
	v_cvt_pk_bf16_f32 v137, v136, v137
	v_cvt_pk_bf16_f32 v136, v140, v141
	v_cvt_pk_bf16_f32 v135, v134, v135
	v_cvt_pk_bf16_f32 v134, v138, v139
	v_pk_fma_f32 v[142:143], v[162:163], v[34:35], v[166:167] op_sel_hi:[0,1,0]
	v_pk_fma_f32 v[138:139], v[162:163], v[36:37], v[166:167] op_sel_hi:[0,1,0]
	v_pk_fma_f32 v[144:145], v[162:163], v[38:39], v[166:167] op_sel_hi:[0,1,0]
	v_pk_fma_f32 v[140:141], v[162:163], v[40:41], v[166:167] op_sel_hi:[0,1,0]
	v_cvt_pk_bf16_f32 v141, v140, v141
	v_cvt_pk_bf16_f32 v140, v144, v145
	v_cvt_pk_bf16_f32 v139, v138, v139
	v_cvt_pk_bf16_f32 v138, v142, v143
	v_pk_fma_f32 v[146:147], v[162:163], v[42:43], v[166:167] op_sel_hi:[0,1,0]
	v_pk_fma_f32 v[142:143], v[162:163], v[44:45], v[166:167] op_sel_hi:[0,1,0]
	v_pk_fma_f32 v[148:149], v[162:163], v[46:47], v[166:167] op_sel_hi:[0,1,0]
	v_pk_fma_f32 v[144:145], v[162:163], v[48:49], v[166:167] op_sel_hi:[0,1,0]
	v_cvt_pk_bf16_f32 v145, v144, v145
	v_cvt_pk_bf16_f32 v144, v148, v149
	v_cvt_pk_bf16_f32 v143, v142, v143
	v_cvt_pk_bf16_f32 v142, v146, v147
	v_pk_fma_f32 v[150:151], v[162:163], v[18:19], v[166:167] op_sel_hi:[0,1,0]
	v_pk_fma_f32 v[146:147], v[162:163], v[20:21], v[166:167] op_sel_hi:[0,1,0]
	v_pk_fma_f32 v[152:153], v[162:163], v[22:23], v[166:167] op_sel_hi:[0,1,0]
	v_pk_fma_f32 v[148:149], v[162:163], v[24:25], v[166:167] op_sel_hi:[0,1,0]
	v_cvt_pk_bf16_f32 v149, v148, v149
	v_cvt_pk_bf16_f32 v148, v152, v153
	v_cvt_pk_bf16_f32 v147, v146, v147
	v_cvt_pk_bf16_f32 v146, v150, v151
	v_pk_fma_f32 v[156:157], v[162:163], v[26:27], v[166:167] op_sel_hi:[0,1,0]
	v_pk_fma_f32 v[150:151], v[162:163], v[28:29], v[166:167] op_sel_hi:[0,1,0]
	v_pk_fma_f32 v[158:159], v[162:163], v[30:31], v[166:167] op_sel_hi:[0,1,0]
	v_pk_fma_f32 v[152:153], v[162:163], v[32:33], v[166:167] op_sel_hi:[0,1,0]
	v_cvt_pk_bf16_f32 v153, v152, v153
	v_cvt_pk_bf16_f32 v152, v158, v159
	v_cvt_pk_bf16_f32 v151, v150, v151
	v_cvt_pk_bf16_f32 v150, v156, v157
	v_pk_fma_f32 v[168:169], v[162:163], v[2:3], v[166:167] op_sel_hi:[0,1,0]
	v_pk_fma_f32 v[156:157], v[162:163], v[4:5], v[166:167] op_sel_hi:[0,1,0]
	v_pk_fma_f32 v[170:171], v[162:163], v[6:7], v[166:167] op_sel_hi:[0,1,0]
	v_pk_fma_f32 v[158:159], v[162:163], v[8:9], v[166:167] op_sel_hi:[0,1,0]
	v_cvt_pk_bf16_f32 v159, v158, v159
	v_cvt_pk_bf16_f32 v158, v170, v171
	v_cvt_pk_bf16_f32 v157, v156, v157
	v_cvt_pk_bf16_f32 v156, v168, v169
	v_pk_fma_f32 v[212:213], v[162:163], v[10:11], v[166:167] op_sel_hi:[0,1,0]
	v_pk_fma_f32 v[208:209], v[162:163], v[12:13], v[166:167] op_sel_hi:[0,1,0]
	v_pk_fma_f32 v[214:215], v[162:163], v[14:15], v[166:167] op_sel_hi:[0,1,0]
	v_pk_fma_f32 v[210:211], v[162:163], v[16:17], v[166:167] op_sel_hi:[0,1,0]
	ds_read_b128 v[166:169], v176
	ds_read_b128 v[170:173], v176 offset:1024
	ds_read_b128 v[182:185], v176 offset:2048
	ds_read_b128 v[188:191], v176 offset:3072
	ds_read_b128 v[192:195], v176 offset:4096
	ds_read_b128 v[196:199], v176 offset:5120
	ds_read_b128 v[200:203], v176 offset:6144
	ds_read_b128 v[204:207], v176 offset:7168
	v_cvt_pk_bf16_f32 v211, v210, v211
	v_cvt_pk_bf16_f32 v210, v214, v215
	v_cvt_pk_bf16_f32 v209, v208, v209
	v_cvt_pk_bf16_f32 v208, v212, v213
	s_waitcnt lgkmcnt(0)
	v_mfma_f32_32x32x16_bf16 v[114:129], v[166:169], v[130:133], v[114:129]
	v_mfma_f32_32x32x16_bf16 v[98:113], v[170:173], v[130:133], v[98:113]
	v_mfma_f32_32x32x16_bf16 v[82:97], v[182:185], v[130:133], v[82:97]
	ds_read_b128 v[166:169], v176 offset:8192
	ds_read_b128 v[170:173], v176 offset:9216
	ds_read_b128 v[182:185], v176 offset:10240
	ds_read_b128 v[212:215], v176 offset:11264
	v_mfma_f32_32x32x16_bf16 v[66:81], v[188:191], v[130:133], v[66:81]
	v_mfma_f32_32x32x16_bf16 v[114:129], v[192:195], v[134:137], v[114:129]
	v_mfma_f32_32x32x16_bf16 v[98:113], v[196:199], v[134:137], v[98:113]
	ds_read_b128 v[130:133], v176 offset:12288
	ds_read_b128 v[188:191], v176 offset:13312
	ds_read_b128 v[192:195], v176 offset:14336
	ds_read_b128 v[196:199], v176 offset:15360
	v_mfma_f32_32x32x16_bf16 v[82:97], v[200:203], v[134:137], v[82:97]
	v_mfma_f32_32x32x16_bf16 v[66:81], v[204:207], v[134:137], v[66:81]
	s_waitcnt lgkmcnt(0)
	v_mfma_f32_32x32x16_bf16 v[114:129], v[166:169], v[138:141], v[114:129]
	v_mfma_f32_32x32x16_bf16 v[98:113], v[170:173], v[138:141], v[98:113]
	v_mfma_f32_32x32x16_bf16 v[82:97], v[182:185], v[138:141], v[82:97]
	v_mfma_f32_32x32x16_bf16 v[66:81], v[212:215], v[138:141], v[66:81]
	s_mov_b64 s[2:3], 0x26000
	v_readfirstlane_b32 s0, v186
	v_mfma_f32_32x32x16_bf16 v[114:129], v[130:133], v[142:145], v[114:129]
	v_lshl_add_u64 v[130:131], v[180:181], 0, s[2:3]
	s_mov_b32 m0, s0
	s_waitcnt vmcnt(4) lgkmcnt(0)
	s_barrier
	global_load_lds_dwordx4 v[130:131], off
	global_load_lds_dwordx4 v[130:131], off offset:1024
	global_load_lds_dwordx4 v[130:131], off offset:2048
	global_load_lds_dwordx4 v[130:131], off offset:3072
	v_mfma_f32_32x32x16_bf16 v[98:113], v[188:191], v[142:145], v[98:113]
	ds_read_b128 v[130:133], v176 offset:20480
	ds_read_b128 v[134:137], v176 offset:21504
	ds_read_b128 v[138:141], v176 offset:22528
	ds_read_b128 v[166:169], v176 offset:23552
	ds_read_b128 v[170:173], v176 offset:24576
	ds_read_b128 v[180:183], v176 offset:25600
	ds_read_b128 v[184:187], v176 offset:26624
	ds_read_b128 v[188:191], v176 offset:27648
	v_mfma_f32_32x32x16_bf16 v[82:97], v[192:195], v[142:145], v[82:97]
	v_mfma_f32_32x32x16_bf16 v[66:81], v[196:199], v[142:145], v[66:81]
	s_waitcnt lgkmcnt(0)
	v_mfma_f32_32x32x16_bf16 v[114:129], v[130:133], v[146:149], v[114:129]
	v_mfma_f32_32x32x16_bf16 v[98:113], v[134:137], v[146:149], v[98:113]
	v_mfma_f32_32x32x16_bf16 v[82:97], v[138:141], v[146:149], v[82:97]
	ds_read_b128 v[130:133], v176 offset:28672
	ds_read_b128 v[134:137], v176 offset:29696
	ds_read_b128 v[138:141], v176 offset:30720
	ds_read_b128 v[142:145], v176 offset:31744
	v_mfma_f32_32x32x16_bf16 v[66:81], v[166:169], v[146:149], v[66:81]
	v_mfma_f32_32x32x16_bf16 v[114:129], v[170:173], v[150:153], v[114:129]
	v_mfma_f32_32x32x16_bf16 v[98:113], v[180:183], v[150:153], v[98:113]
	ds_read_b128 v[146:149], v176 offset:32768
	ds_read_b128 v[166:169], v176 offset:33792
	ds_read_b128 v[170:173], v176 offset:34816
	ds_read_b128 v[180:183], v176 offset:35840
	v_mfma_f32_32x32x16_bf16 v[82:97], v[184:187], v[150:153], v[82:97]
	v_mfma_f32_32x32x16_bf16 v[66:81], v[188:191], v[150:153], v[66:81]
	s_waitcnt lgkmcnt(0)
	v_mfma_f32_32x32x16_bf16 v[114:129], v[130:133], v[156:159], v[114:129]
	v_mfma_f32_32x32x16_bf16 v[98:113], v[134:137], v[156:159], v[98:113]
	v_mfma_f32_32x32x16_bf16 v[82:97], v[138:141], v[156:159], v[82:97]
	v_mfma_f32_32x32x16_bf16 v[66:81], v[142:145], v[156:159], v[66:81]
	v_mfma_f32_32x32x16_bf16 v[114:129], v[146:149], v[208:211], v[114:129]
	s_waitcnt vmcnt(4) lgkmcnt(0)
	s_barrier
	v_mfma_f32_32x32x16_bf16 v[98:113], v[166:169], v[208:211], v[98:113]
	s_nop 8
	v_mul_f32_e32 v130, 0x3c23d70a, v114
	v_mul_f32_e32 v131, 0x3c23d70a, v115
	v_max_f32_e32 v114, v114, v130
	v_mul_f32_e32 v130, 0x3c23d70a, v116
	v_max_f32_e32 v115, v115, v131
	v_max_f32_e32 v116, v116, v130
	v_mul_f32_e32 v130, 0x3c23d70a, v117
	v_max_f32_e32 v117, v117, v130
	v_cvt_pk_bf16_f32 v134, v114, v115
	v_mul_f32_e32 v114, 0x3c23d70a, v122
	v_cvt_pk_bf16_f32 v135, v116, v117
	v_max_f32_e32 v114, v122, v114
	v_mul_f32_e32 v115, 0x3c23d70a, v123
	v_mfma_f32_32x32x16_bf16 v[82:97], v[170:173], v[208:211], v[82:97]
	v_max_f32_e32 v115, v123, v115
	v_cvt_pk_bf16_f32 v138, v114, v115
	v_mul_f32_e32 v114, 0x3c23d70a, v98
	v_max_f32_e32 v98, v98, v114
	v_mul_f32_e32 v114, 0x3c23d70a, v99
	v_max_f32_e32 v99, v99, v114
	v_mul_f32_e32 v114, 0x3c23d70a, v100
	v_max_f32_e32 v100, v100, v114
	v_mul_f32_e32 v114, 0x3c23d70a, v101
	v_max_f32_e32 v101, v101, v114
	v_cvt_pk_bf16_f32 v142, v98, v99
	v_mul_f32_e32 v98, 0x3c23d70a, v106
	v_cvt_pk_bf16_f32 v143, v100, v101
	v_max_f32_e32 v98, v106, v98
	v_mul_f32_e32 v99, 0x3c23d70a, v107
	v_mfma_f32_32x32x16_bf16 v[66:81], v[180:183], v[208:211], v[66:81]
	v_max_f32_e32 v99, v107, v99
	v_cvt_pk_bf16_f32 v146, v98, v99
	v_mul_f32_e32 v98, 0x3c23d70a, v82
	v_max_f32_e32 v82, v82, v98
	v_mul_f32_e32 v98, 0x3c23d70a, v83
	v_max_f32_e32 v83, v83, v98
	v_mul_f32_e32 v98, 0x3c23d70a, v84
	v_max_f32_e32 v84, v84, v98
	v_mul_f32_e32 v98, 0x3c23d70a, v85
	v_max_f32_e32 v85, v85, v98
	v_cvt_pk_bf16_f32 v150, v82, v83
	v_mul_f32_e32 v82, 0x3c23d70a, v90
	v_cvt_pk_bf16_f32 v151, v84, v85
	v_max_f32_e32 v82, v90, v82
	v_mul_f32_e32 v83, 0x3c23d70a, v91
	v_max_f32_e32 v83, v91, v83
	v_mul_f32_e32 v130, 0x3c23d70a, v118
	v_cvt_pk_bf16_f32 v156, v82, v83
	v_mul_f32_e32 v82, 0x3c23d70a, v66
	v_max_f32_e32 v118, v118, v130
	v_mul_f32_e32 v130, 0x3c23d70a, v119
	v_max_f32_e32 v66, v66, v82
	v_mul_f32_e32 v82, 0x3c23d70a, v67
	v_max_f32_e32 v119, v119, v130
	v_mul_f32_e32 v130, 0x3c23d70a, v120
	v_mul_f32_e32 v114, 0x3c23d70a, v102
	v_mul_f32_e32 v98, 0x3c23d70a, v86
	v_max_f32_e32 v67, v67, v82
	v_max_f32_e32 v120, v120, v130
	v_mul_f32_e32 v130, 0x3c23d70a, v121
	v_max_f32_e32 v102, v102, v114
	v_mul_f32_e32 v114, 0x3c23d70a, v103
	v_max_f32_e32 v86, v86, v98
	v_mul_f32_e32 v98, 0x3c23d70a, v87
	v_cvt_pk_bf16_f32 v166, v66, v67
	v_mul_f32_e32 v66, 0x3c23d70a, v74
	v_max_f32_e32 v121, v121, v130
	v_mul_f32_e32 v116, 0x3c23d70a, v124
	v_max_f32_e32 v103, v103, v114
	v_mul_f32_e32 v114, 0x3c23d70a, v104
	v_mul_f32_e32 v100, 0x3c23d70a, v108
	v_max_f32_e32 v87, v87, v98
	v_mul_f32_e32 v98, 0x3c23d70a, v88
	v_mul_f32_e32 v84, 0x3c23d70a, v92
	v_mul_f32_e32 v82, 0x3c23d70a, v68
	v_max_f32_e32 v130, v74, v66
	v_mul_f32_e32 v66, 0x3c23d70a, v75
	v_cvt_pk_bf16_f32 v136, v118, v119
	v_max_f32_e32 v116, v124, v116
	v_mul_f32_e32 v117, 0x3c23d70a, v125
	v_max_f32_e32 v104, v104, v114
	v_mul_f32_e32 v114, 0x3c23d70a, v105
	v_cvt_pk_bf16_f32 v144, v102, v103
	v_max_f32_e32 v100, v108, v100
	v_mul_f32_e32 v101, 0x3c23d70a, v109
	v_max_f32_e32 v88, v88, v98
	v_mul_f32_e32 v98, 0x3c23d70a, v89
	v_cvt_pk_bf16_f32 v152, v86, v87
	v_max_f32_e32 v84, v92, v84
	v_mul_f32_e32 v85, 0x3c23d70a, v93
	v_max_f32_e32 v68, v68, v82
	v_mul_f32_e32 v82, 0x3c23d70a, v69
	v_max_f32_e32 v155, v75, v66
	v_mul_f32_e32 v66, 0x3c23d70a, v76
	v_max_f32_e32 v117, v125, v117
	v_mul_f32_e32 v118, 0x3c23d70a, v126
	v_max_f32_e32 v105, v105, v114
	v_max_f32_e32 v101, v109, v101
	v_mul_f32_e32 v102, 0x3c23d70a, v110
	v_max_f32_e32 v89, v89, v98
	v_max_f32_e32 v85, v93, v85
	v_mul_f32_e32 v86, 0x3c23d70a, v94
	v_max_f32_e32 v69, v69, v82
	v_mul_f32_e32 v82, 0x3c23d70a, v70
	v_max_f32_e32 v131, v76, v66
	v_mul_f32_e32 v66, 0x3c23d70a, v77
	v_cvt_pk_bf16_f32 v137, v120, v121
	v_max_f32_e32 v118, v126, v118
	v_mul_f32_e32 v119, 0x3c23d70a, v127
	v_cvt_pk_bf16_f32 v145, v104, v105
	v_max_f32_e32 v102, v110, v102
	v_mul_f32_e32 v103, 0x3c23d70a, v111
	v_cvt_pk_bf16_f32 v153, v88, v89
	v_max_f32_e32 v86, v94, v86
	v_mul_f32_e32 v87, 0x3c23d70a, v95
	v_max_f32_e32 v70, v70, v82
	v_mul_f32_e32 v82, 0x3c23d70a, v71
	v_max_f32_e32 v162, v77, v66
	v_mul_f32_e32 v66, 0x3c23d70a, v78
	v_max_f32_e32 v119, v127, v119
	v_mul_f32_e32 v120, 0x3c23d70a, v128
	v_max_f32_e32 v103, v111, v103
	v_mul_f32_e32 v104, 0x3c23d70a, v112
	v_max_f32_e32 v87, v95, v87
	v_mul_f32_e32 v88, 0x3c23d70a, v96
	v_max_f32_e32 v71, v71, v82
	v_mul_f32_e32 v82, 0x3c23d70a, v72
	v_max_f32_e32 v132, v78, v66
	v_mul_f32_e32 v66, 0x3c23d70a, v79
	v_max_f32_e32 v120, v128, v120
	v_mul_f32_e32 v121, 0x3c23d70a, v129
	v_max_f32_e32 v104, v112, v104
	v_mul_f32_e32 v105, 0x3c23d70a, v113
	v_max_f32_e32 v88, v96, v88
	v_mul_f32_e32 v89, 0x3c23d70a, v97
	v_max_f32_e32 v72, v72, v82
	v_mul_f32_e32 v82, 0x3c23d70a, v73
	v_max_f32_e32 v174, v79, v66
	v_mul_f32_e32 v66, 0x3c23d70a, v80
	v_max_f32_e32 v121, v129, v121
	v_max_f32_e32 v105, v113, v105
	v_max_f32_e32 v89, v97, v89
	v_max_f32_e32 v73, v73, v82
	v_max_f32_e32 v133, v80, v66
	v_mul_f32_e32 v66, 0x3c23d70a, v81
	v_cvt_pk_bf16_f32 v141, v120, v121
	v_cvt_pk_bf16_f32 v140, v118, v119
	v_cvt_pk_bf16_f32 v139, v116, v117
	v_cvt_pk_bf16_f32 v149, v104, v105
	v_cvt_pk_bf16_f32 v148, v102, v103
	v_cvt_pk_bf16_f32 v147, v100, v101
	v_cvt_pk_bf16_f32 v159, v88, v89
	v_cvt_pk_bf16_f32 v158, v86, v87
	v_cvt_pk_bf16_f32 v157, v84, v85
	v_cvt_pk_bf16_f32 v169, v72, v73
	v_cvt_pk_bf16_f32 v168, v70, v71
	v_cvt_pk_bf16_f32 v167, v68, v69
	v_max_f32_e32 v177, v81, v66
	ds_read_b128 v[114:117], v154 offset:59392
	ds_read_b128 v[118:121], v154 offset:59424
	ds_read_b128 v[122:125], v154 offset:59456
	ds_read_b128 v[126:129], v154 offset:59488
	ds_read_b128 v[98:101], v154 offset:59520
	ds_read_b128 v[102:105], v154 offset:59552
	ds_read_b128 v[106:109], v154 offset:59584
	ds_read_b128 v[110:113], v154 offset:59616
	ds_read_b128 v[82:85], v154 offset:59648
	ds_read_b128 v[86:89], v154 offset:59680
	ds_read_b128 v[90:93], v154 offset:59712
	ds_read_b128 v[94:97], v154 offset:59744
	ds_read_b128 v[66:69], v154 offset:59776
	ds_read_b128 v[70:73], v154 offset:59808
	ds_read_b128 v[74:77], v154 offset:59840
	ds_read_b128 v[78:81], v154 offset:59872
	ds_read_b128 v[170:173], v176 offset:40960
	ds_read_b128 v[180:183], v176 offset:41984
	ds_read_b128 v[184:187], v176 offset:43008
	ds_read_b128 v[188:191], v176 offset:44032
	ds_read_b128 v[192:195], v176 offset:45056
	ds_read_b128 v[196:199], v176 offset:46080
	ds_read_b128 v[200:203], v176 offset:47104
	ds_read_b128 v[204:207], v176 offset:48128
	v_cvt_pk_bf16_f32 v133, v133, v177
	v_cvt_pk_bf16_f32 v132, v132, v174
	v_cvt_pk_bf16_f32 v131, v131, v162
	v_cvt_pk_bf16_f32 v130, v130, v155
	s_waitcnt lgkmcnt(0)
	v_mfma_f32_32x32x16_bf16 v[114:129], v[170:173], v[134:137], v[114:129]
	v_mfma_f32_32x32x16_bf16 v[98:113], v[180:183], v[134:137], v[98:113]
	v_mfma_f32_32x32x16_bf16 v[82:97], v[184:187], v[134:137], v[82:97]
	ds_read_b128 v[170:173], v176 offset:49152
	ds_read_b128 v[180:183], v176 offset:50176
	ds_read_b128 v[184:187], v176 offset:51200
	ds_read_b128 v[208:211], v176 offset:52224
	v_mfma_f32_32x32x16_bf16 v[66:81], v[188:191], v[134:137], v[66:81]
	v_mfma_f32_32x32x16_bf16 v[114:129], v[192:195], v[138:141], v[114:129]
	v_mfma_f32_32x32x16_bf16 v[98:113], v[196:199], v[138:141], v[98:113]
	ds_read_b128 v[134:137], v176 offset:53248
	ds_read_b128 v[188:191], v176 offset:54272
	ds_read_b128 v[192:195], v176 offset:55296
	ds_read_b128 v[196:199], v176 offset:56320
	v_mfma_f32_32x32x16_bf16 v[82:97], v[200:203], v[138:141], v[82:97]
	v_mfma_f32_32x32x16_bf16 v[66:81], v[204:207], v[138:141], v[66:81]
	s_waitcnt lgkmcnt(0)
	v_mfma_f32_32x32x16_bf16 v[114:129], v[170:173], v[142:145], v[114:129]
	v_mfma_f32_32x32x16_bf16 v[98:113], v[180:183], v[142:145], v[98:113]
	v_mfma_f32_32x32x16_bf16 v[82:97], v[184:187], v[142:145], v[82:97]
	v_mfma_f32_32x32x16_bf16 v[66:81], v[208:211], v[142:145], v[66:81]
	v_mfma_f32_32x32x16_bf16 v[114:129], v[134:137], v[146:149], v[114:129]
	s_waitcnt vmcnt(0) lgkmcnt(0)
	s_barrier
	v_mfma_f32_32x32x16_bf16 v[98:113], v[188:191], v[146:149], v[98:113]
	v_mfma_f32_32x32x16_bf16 v[82:97], v[192:195], v[146:149], v[82:97]
	ds_read_b128 v[134:137], v176
	ds_read_b128 v[138:141], v176 offset:1024
	ds_read_b128 v[142:145], v176 offset:2048
	ds_read_b128 v[170:173], v176 offset:3072
	ds_read_b128 v[180:183], v176 offset:4096
	ds_read_b128 v[184:187], v176 offset:5120
	ds_read_b128 v[188:191], v176 offset:6144
	ds_read_b128 v[192:195], v176 offset:7168
	v_mfma_f32_32x32x16_bf16 v[66:81], v[196:199], v[146:149], v[66:81]
	s_waitcnt lgkmcnt(5)
	v_mfma_f32_32x32x16_bf16 v[82:97], v[142:145], v[150:153], v[82:97]
	ds_read_b128 v[142:145], v176 offset:8192
	ds_read_b128 v[146:149], v176 offset:9216
	ds_read_b128 v[196:199], v176 offset:10240
	ds_read_b128 v[200:203], v176 offset:11264
	v_mfma_f32_32x32x16_bf16 v[114:129], v[134:137], v[150:153], v[114:129]
	v_mfma_f32_32x32x16_bf16 v[98:113], v[138:141], v[150:153], v[98:113]
	s_waitcnt lgkmcnt(8)
	v_mfma_f32_32x32x16_bf16 v[66:81], v[170:173], v[150:153], v[66:81]
	ds_read_b128 v[150:153], v176 offset:12288
	ds_read_b128 v[170:173], v176 offset:13312
	ds_read_b128 v[138:141], v176 offset:14336
	ds_read_b128 v[134:137], v176 offset:15360
	s_waitcnt lgkmcnt(11)
	v_mfma_f32_32x32x16_bf16 v[114:129], v[180:183], v[156:159], v[114:129]
	s_waitcnt lgkmcnt(10)
	v_mfma_f32_32x32x16_bf16 v[98:113], v[184:187], v[156:159], v[98:113]
	s_waitcnt lgkmcnt(9)
	v_mfma_f32_32x32x16_bf16 v[82:97], v[188:191], v[156:159], v[82:97]
	s_waitcnt lgkmcnt(8)
	v_mfma_f32_32x32x16_bf16 v[66:81], v[192:195], v[156:159], v[66:81]
	s_waitcnt lgkmcnt(7)
	v_mfma_f32_32x32x16_bf16 v[114:129], v[142:145], v[166:169], v[114:129]
	s_waitcnt lgkmcnt(6)
	v_mfma_f32_32x32x16_bf16 v[98:113], v[146:149], v[166:169], v[98:113]
	s_waitcnt lgkmcnt(5)
	v_mfma_f32_32x32x16_bf16 v[82:97], v[196:199], v[166:169], v[82:97]
	s_waitcnt lgkmcnt(4)
	v_mfma_f32_32x32x16_bf16 v[66:81], v[200:203], v[166:169], v[66:81]
	s_waitcnt lgkmcnt(3)
	v_mfma_f32_32x32x16_bf16 v[114:129], v[150:153], v[130:133], v[114:129]
	v_and_b32_e32 v0, 7, v0
	v_lshlrev_b32_e32 v174, 4, v0
	v_or_b32_e32 v144, v1, v174
	v_mad_u32_u24 v145, v161, s1, v144
	v_lshl_add_u64 v[142:143], s[6:7], 0, v[178:179]
	s_nop 6
	v_mul_f32_e32 v0, 0x3c23d70a, v114
	v_max_f32_e32 v0, v114, v0
	v_mul_f32_e32 v1, 0x3c23d70a, v115
	v_max_f32_e32 v1, v115, v1
	v_pk_add_f32 v[50:51], v[50:51], v[0:1]
	v_mul_f32_e32 v0, 0x3c23d70a, v116
	v_max_f32_e32 v0, v116, v0
	v_mul_f32_e32 v1, 0x3c23d70a, v117
	v_max_f32_e32 v114, v117, v117
	v_max_f32_e32 v1, v114, v1
	v_pk_add_f32 v[52:53], v[52:53], v[0:1]
	v_mul_f32_e32 v0, 0x3c23d70a, v118
	ds_write_b128 v160, v[50:53] offset:61440
	v_max_f32_e32 v0, v118, v0
	v_mul_f32_e32 v1, 0x3c23d70a, v119
	v_max_f32_e32 v1, v119, v1
	v_pk_add_f32 v[50:51], v[54:55], v[0:1]
	v_mul_f32_e32 v0, 0x3c23d70a, v120
	v_max_f32_e32 v0, v120, v0
	v_mul_f32_e32 v1, 0x3c23d70a, v121
	v_max_f32_e32 v1, v121, v1
	v_pk_add_f32 v[52:53], v[56:57], v[0:1]
	v_mul_f32_e32 v0, 0x3c23d70a, v122
	ds_write_b128 v160, v[50:53] offset:61472
	v_max_f32_e32 v0, v122, v0
	v_mul_f32_e32 v1, 0x3c23d70a, v123
	v_max_f32_e32 v1, v123, v1
	v_pk_add_f32 v[50:51], v[58:59], v[0:1]
	v_mul_f32_e32 v0, 0x3c23d70a, v124
	v_max_f32_e32 v0, v124, v0
	v_mul_f32_e32 v1, 0x3c23d70a, v125
	v_max_f32_e32 v1, v125, v1
	v_pk_add_f32 v[52:53], v[60:61], v[0:1]
	v_mul_f32_e32 v0, 0x3c23d70a, v126
	ds_write_b128 v160, v[50:53] offset:61504
	v_max_f32_e32 v0, v126, v0
	v_mul_f32_e32 v1, 0x3c23d70a, v127
	v_max_f32_e32 v1, v127, v1
	v_pk_add_f32 v[50:51], v[62:63], v[0:1]
	v_mul_f32_e32 v0, 0x3c23d70a, v128
	v_max_f32_e32 v0, v128, v0
	v_mul_f32_e32 v1, 0x3c23d70a, v129
	v_max_f32_e32 v1, v129, v1
	v_pk_add_f32 v[52:53], v[64:65], v[0:1]
	ds_write_b128 v160, v[50:53] offset:61536
	ds_read_b128 v[50:53], v145 offset:61440
	v_add_u32_e32 v62, v144, v165
	ds_read_b128 v[54:57], v62 offset:61440
	v_lshl_add_u64 v[142:143], v[142:143], 0, v[174:175]
	v_lshlrev_b32_e32 v174, 9, v161
	s_waitcnt lgkmcnt(8)
	v_mfma_f32_32x32x16_bf16 v[98:113], v[170:173], v[130:133], v[98:113]
	v_lshl_add_u64 v[0:1], v[142:143], 0, v[174:175]
	s_waitcnt lgkmcnt(1)
	global_store_dwordx4 v[0:1], v[50:53], off sc1
	v_add_u32_e32 v63, v144, v164
	v_add_u32_e32 v64, v144, v163
	v_or_b32_e32 v50, 0x1000, v174
	v_mov_b32_e32 v51, v175
	v_lshl_add_u64 v[50:51], v[142:143], 0, v[50:51]
	ds_read_b128 v[58:61], v64 offset:61440
	s_waitcnt lgkmcnt(1)
	global_store_dwordx4 v[50:51], v[54:57], off sc1
	ds_read_b128 v[54:57], v63 offset:61440
	v_or_b32_e32 v52, 0x2000, v174
	v_mov_b32_e32 v53, v175
	v_lshl_add_u64 v[52:53], v[142:143], 0, v[52:53]
	v_or_b32_e32 v174, 0x3000, v174
	s_waitcnt lgkmcnt(0)
	global_store_dwordx4 v[52:53], v[54:57], off sc1
	v_mfma_f32_32x32x16_bf16 v[82:97], v[138:141], v[130:133], v[82:97]
	s_nop 0
	v_lshl_add_u64 v[54:55], v[142:143], 0, v[174:175]
	v_mul_f32_e32 v56, 0x3c23d70a, v98
	global_store_dwordx4 v[54:55], v[58:61], off sc1
	v_max_f32_e32 v56, v98, v56
	v_mul_f32_e32 v57, 0x3c23d70a, v99
	v_max_f32_e32 v57, v99, v57
	v_pk_add_f32 v[34:35], v[34:35], v[56:57]
	v_mul_f32_e32 v56, 0x3c23d70a, v100
	v_max_f32_e32 v56, v100, v56
	v_mul_f32_e32 v57, 0x3c23d70a, v101
	v_max_f32_e32 v58, v101, v101
	v_max_f32_e32 v57, v58, v57
	v_pk_add_f32 v[36:37], v[36:37], v[56:57]
	ds_write_b128 v160, v[34:37] offset:61440
	v_mul_f32_e32 v34, 0x3c23d70a, v102
	v_max_f32_e32 v34, v102, v34
	v_mul_f32_e32 v35, 0x3c23d70a, v103
	v_max_f32_e32 v35, v103, v35
	v_mul_f32_e32 v36, 0x3c23d70a, v104
	v_pk_add_f32 v[34:35], v[38:39], v[34:35]
	v_max_f32_e32 v36, v104, v36
	v_mul_f32_e32 v37, 0x3c23d70a, v105
	v_max_f32_e32 v37, v105, v37
	v_pk_add_f32 v[36:37], v[40:41], v[36:37]
	ds_write_b128 v160, v[34:37] offset:61472
	v_mul_f32_e32 v34, 0x3c23d70a, v106
	v_max_f32_e32 v34, v106, v34
	v_mul_f32_e32 v35, 0x3c23d70a, v107
	v_max_f32_e32 v35, v107, v35
	v_mul_f32_e32 v36, 0x3c23d70a, v108
	v_max_f32_e32 v36, v108, v36
	v_mul_f32_e32 v37, 0x3c23d70a, v109
	v_max_f32_e32 v37, v109, v37
	v_pk_add_f32 v[34:35], v[42:43], v[34:35]
	v_pk_add_f32 v[36:37], v[44:45], v[36:37]
	ds_write_b128 v160, v[34:37] offset:61504
	v_mul_f32_e32 v34, 0x3c23d70a, v110
	v_max_f32_e32 v34, v110, v34
	v_mul_f32_e32 v35, 0x3c23d70a, v111
	v_max_f32_e32 v35, v111, v35
	v_mul_f32_e32 v36, 0x3c23d70a, v112
	v_max_f32_e32 v36, v112, v36
	v_mul_f32_e32 v37, 0x3c23d70a, v113
	v_max_f32_e32 v37, v113, v37
	v_pk_add_f32 v[34:35], v[46:47], v[34:35]
	v_pk_add_f32 v[36:37], v[48:49], v[36:37]
	ds_write_b128 v160, v[34:37] offset:61536
	ds_read_b128 v[34:37], v145 offset:61440
	ds_read_b128 v[38:41], v62 offset:61440
	ds_read_b128 v[42:45], v63 offset:61440
	ds_read_b128 v[46:49], v64 offset:61440
	s_waitcnt lgkmcnt(3)
	global_store_dwordx4 v[0:1], v[34:37], off offset:128 sc1
	s_waitcnt lgkmcnt(2)
	global_store_dwordx4 v[50:51], v[38:41], off offset:128 sc1
	s_waitcnt lgkmcnt(1)
	global_store_dwordx4 v[52:53], v[42:45], off offset:128 sc1
	s_waitcnt lgkmcnt(0)
	global_store_dwordx4 v[54:55], v[46:49], off offset:128 sc1
	v_mul_f32_e32 v34, 0x3c23d70a, v82
	v_max_f32_e32 v34, v82, v34
	v_mul_f32_e32 v35, 0x3c23d70a, v83
	v_max_f32_e32 v35, v83, v35
	v_pk_add_f32 v[18:19], v[18:19], v[34:35]
	v_mul_f32_e32 v34, 0x3c23d70a, v84
	v_max_f32_e32 v34, v84, v34
	v_mul_f32_e32 v35, 0x3c23d70a, v85
	v_max_f32_e32 v36, v85, v85
	v_max_f32_e32 v35, v36, v35
	v_pk_add_f32 v[20:21], v[20:21], v[34:35]
	ds_write_b128 v160, v[18:21] offset:61440
	v_mul_f32_e32 v18, 0x3c23d70a, v86
	v_max_f32_e32 v18, v86, v18
	v_mul_f32_e32 v19, 0x3c23d70a, v87
	v_max_f32_e32 v19, v87, v19
	v_mul_f32_e32 v20, 0x3c23d70a, v88
	v_pk_add_f32 v[18:19], v[22:23], v[18:19]
	v_max_f32_e32 v20, v88, v20
	v_mul_f32_e32 v21, 0x3c23d70a, v89
	v_max_f32_e32 v21, v89, v21
	v_pk_add_f32 v[20:21], v[24:25], v[20:21]
	ds_write_b128 v160, v[18:21] offset:61472
	v_mul_f32_e32 v18, 0x3c23d70a, v90
	v_max_f32_e32 v18, v90, v18
	v_mul_f32_e32 v19, 0x3c23d70a, v91
	v_max_f32_e32 v19, v91, v19
	v_mul_f32_e32 v20, 0x3c23d70a, v92
	v_max_f32_e32 v20, v92, v20
	v_mul_f32_e32 v21, 0x3c23d70a, v93
	v_max_f32_e32 v21, v93, v21
	v_pk_add_f32 v[18:19], v[26:27], v[18:19]
	v_pk_add_f32 v[20:21], v[28:29], v[20:21]
	ds_write_b128 v160, v[18:21] offset:61504
	v_mul_f32_e32 v18, 0x3c23d70a, v94
	v_max_f32_e32 v18, v94, v18
	v_mul_f32_e32 v19, 0x3c23d70a, v95
	v_max_f32_e32 v19, v95, v19
	v_mul_f32_e32 v20, 0x3c23d70a, v96
	v_max_f32_e32 v20, v96, v20
	v_mul_f32_e32 v21, 0x3c23d70a, v97
	v_mfma_f32_32x32x16_bf16 v[66:81], v[134:137], v[130:133], v[66:81]
	v_max_f32_e32 v21, v97, v21
	v_add_f32_e64 v18, v30, v18
	v_add_f32_e64 v19, v31, v19
	v_add_f32_e64 v20, v32, v20
	v_add_f32_e64 v21, v33, v21
	ds_write_b128 v160, v[18:21] offset:61536
	ds_read_b128 v[18:21], v145 offset:61440
	ds_read_b128 v[22:25], v62 offset:61440
	ds_read_b128 v[26:29], v63 offset:61440
	ds_read_b128 v[30:33], v64 offset:61440
	s_waitcnt lgkmcnt(3)
	global_store_dwordx4 v[0:1], v[18:21], off offset:256 sc1
	s_waitcnt lgkmcnt(2)
	global_store_dwordx4 v[50:51], v[22:25], off offset:256 sc1
	s_waitcnt lgkmcnt(1)
	global_store_dwordx4 v[52:53], v[26:29], off offset:256 sc1
	s_waitcnt lgkmcnt(0)
	global_store_dwordx4 v[54:55], v[30:33], off offset:256 sc1
	v_mul_f32_e32 v18, 0x3c23d70a, v66
	v_max_f32_e32 v18, v66, v18
	v_mul_f32_e32 v19, 0x3c23d70a, v67
	v_max_f32_e32 v19, v67, v19
	v_pk_add_f32 v[2:3], v[2:3], v[18:19]
	v_mul_f32_e32 v18, 0x3c23d70a, v68
	v_max_f32_e32 v18, v68, v18
	v_mul_f32_e32 v19, 0x3c23d70a, v69
	v_max_f32_e32 v20, v69, v69
	v_max_f32_e32 v19, v20, v19
	v_pk_add_f32 v[4:5], v[4:5], v[18:19]
	ds_write_b128 v160, v[2:5] offset:61440
	v_mul_f32_e32 v2, 0x3c23d70a, v70
	v_max_f32_e32 v2, v70, v2
	v_mul_f32_e32 v3, 0x3c23d70a, v71
	v_max_f32_e32 v3, v71, v3
	v_mul_f32_e32 v4, 0x3c23d70a, v72
	v_pk_add_f32 v[2:3], v[6:7], v[2:3]
	v_max_f32_e32 v4, v72, v4
	v_mul_f32_e32 v5, 0x3c23d70a, v73
	v_max_f32_e32 v5, v73, v5
	v_pk_add_f32 v[4:5], v[8:9], v[4:5]
	ds_write_b128 v160, v[2:5] offset:61472
	v_mul_f32_e32 v2, 0x3c23d70a, v74
	v_max_f32_e32 v2, v74, v2
	v_mul_f32_e32 v3, 0x3c23d70a, v75
	v_max_f32_e32 v3, v75, v3
	v_mul_f32_e32 v4, 0x3c23d70a, v76
	v_max_f32_e32 v4, v76, v4
	v_mul_f32_e32 v5, 0x3c23d70a, v77
	v_max_f32_e32 v5, v77, v5
	v_pk_add_f32 v[2:3], v[10:11], v[2:3]
	v_pk_add_f32 v[4:5], v[12:13], v[4:5]
	ds_write_b128 v160, v[2:5] offset:61504
	v_mul_f32_e32 v2, 0x3c23d70a, v78
	v_max_f32_e32 v2, v78, v2
	v_mul_f32_e32 v3, 0x3c23d70a, v79
	v_max_f32_e32 v3, v79, v3
	v_mul_f32_e32 v4, 0x3c23d70a, v80
	v_max_f32_e32 v4, v80, v4
	v_mul_f32_e32 v5, 0x3c23d70a, v81
	v_max_f32_e32 v5, v81, v5
	v_pk_add_f32 v[2:3], v[14:15], v[2:3]
	v_pk_add_f32 v[4:5], v[16:17], v[4:5]
	ds_write_b128 v160, v[2:5] offset:61536
	ds_read_b128 v[2:5], v145 offset:61440
	ds_read_b128 v[6:9], v62 offset:61440
	ds_read_b128 v[10:13], v63 offset:61440
	ds_read_b128 v[14:17], v64 offset:61440
	s_waitcnt lgkmcnt(3)
	global_store_dwordx4 v[0:1], v[2:5], off offset:384 sc1
	s_waitcnt lgkmcnt(2)
	global_store_dwordx4 v[50:51], v[6:9], off offset:384 sc1
	s_waitcnt lgkmcnt(1)
	global_store_dwordx4 v[52:53], v[10:13], off offset:384 sc1
	s_waitcnt lgkmcnt(0)
	global_store_dwordx4 v[54:55], v[14:17], off offset:384 sc1
	s_endpgm

_Z16node_post_kernelPKfS0_PKtS0_S2_S0_S0_S0_S0_S0_Pf:
	s_load_dwordx16 s[4:19], s[0:1], 0x0
	s_load_dwordx4 s[20:23], s[0:1], 0x40
	s_load_dwordx2 s[24:25], s[0:1], 0x50
	v_lshrrev_b32_e32 v5, 6, v0
	v_and_b32_e32 v1, 63, v0
	v_and_b32_e32 v2, 15, v0
	v_bfe_u32 v3, v0, 4, 2
	v_readfirstlane_b32 s26, v5
	v_lshlrev_b32_e32 v4, 4, v1
	v_lshlrev_b32_e32 v6, 5, v1
	v_add_u32_e32 v7, 0x1000, v6
	v_lshlrev_b32_e32 v8, 2, v1
	v_add_u32_e32 v9, 0x1000, v4
	v_add_u32_e32 v10, 0x2000, v4
	v_add_u32_e32 v11, 0x3000, v4
	v_lshlrev_b32_e32 v12, 7, v5
	v_lshl_or_b32 v12, v3, 4, v12
	v_and_b32_e32 v13, 1, v2
	v_lshl_or_b32 v13, v13, 10, v12
	v_mov_b32_e32 v14, 0xff7fffff
	v_cmp_gt_u32_e64 s[58:59], 2, v2
	s_lshl_b32 s27, s2, 1
	s_lshr_b32 s28, s2, 7
	s_and_b32 s29, s26, 1
	s_add_u32 s32, s27, s29
	s_lshl_b32 s32, s32, 13
	s_lshr_b32 s33, s26, 1
	s_lshl_b32 s33, s33, 3
	s_add_u32 s32, s32, s33
	s_lshl_b32 s60, s26, 14
	s_lshl_b32 s61, s28, 17
	s_add_u32 s61, s61, s60
	s_lshl_b32 s62, s28, 10
	s_lshl_b32 s63, s27, 10
	s_waitcnt lgkmcnt(0)
	s_add_u32 s30, s4, s32
	s_addc_u32 s31, s5, 0
	s_add_u32 s34, s6, s62
	s_addc_u32 s35, s7, 0
	s_add_u32 s36, s8, s61
	s_addc_u32 s37, s9, 0
	s_add_u32 s38, s12, s60
	s_addc_u32 s39, s13, 0
	s_add_u32 s40, s38, 0x20000
	s_addc_u32 s41, s39, 0
	s_add_u32 s42, s38, 0x40000
	s_addc_u32 s43, s39, 0
	s_add_u32 s44, s10, s63
	s_addc_u32 s45, s11, 0
	s_add_u32 s46, s24, s63
	s_addc_u32 s47, s25, 0
	global_load_dwordx2 v[56:57], v6, s[30:31]
	global_load_dwordx2 v[58:59], v6, s[30:31] offset:2048
	global_load_dwordx2 v[60:61], v7, s[30:31]
	global_load_dwordx2 v[62:63], v7, s[30:31] offset:2048
	global_load_dword v40, v8, s[34:35]
	global_load_dword v41, v8, s[34:35] offset:256
	global_load_dword v42, v8, s[34:35] offset:512
	global_load_dword v43, v8, s[34:35] offset:768
	s_lshr_b32 s64, s2, 3
	s_and_b32 s64, s64, 31
	s_and_b32 s65, s64, 15
	s_lshl_b32 s65, s65, 13
	s_lshl_b32 s66, s28, 17
	s_add_u32 s65, s65, s66
	s_lshl_b32 s67, s26, 10
	s_add_u32 s65, s65, s67
	s_add_u32 s68, s8, s65
	s_addc_u32 s69, s9, 0
	s_mul_i32 s66, s64, 0x3000
	s_lshl_b32 s67, s26, 11
	s_min_u32 s67, s67, 0x2800
	s_add_u32 s66, s66, s67
	s_add_u32 s70, s12, s66
	s_addc_u32 s71, s13, 0
	global_load_dwordx4 v[192:195], v4, s[68:69]
	global_load_dwordx4 v[196:199], v4, s[70:71]
	global_load_dwordx4 v[200:203], v4, s[70:71] offset:1024
	global_load_dwordx4 v[16:19], v12, s[14:15]
	global_load_dwordx4 v[20:23], v12, s[14:15] offset:64
	global_load_dwordx4 v[24:27], v13, s[44:45]
	global_load_dwordx4 v[28:31], v13, s[44:45] offset:64
	global_load_dwordx4 v[32:35], v4, s[16:17]
	global_load_dwordx4 v[36:39], v4, s[18:19]
	v_lshlrev_b32_e32 v15, 1, v1
	s_lshl_b32 s48, s29, 12
	s_lshl_b32 s49, s33, 7
	s_add_u32 s48, s48, s49
	v_add_u32_e32 v15, s48, v15
	s_waitcnt vmcnt(9)
	v_cmp_neq_f32_e64 s[50:51], 0, v40
	v_cmp_neq_f32_e64 s[52:53], 0, v41
	v_cmp_neq_f32_e64 s[54:55], 0, v42
	v_cmp_neq_f32_e64 s[56:57], 0, v43
	v_cndmask_b32_e64 v56, v14, v56, s[50:51]
	v_cndmask_b32_e64 v57, v14, v57, s[50:51]
	v_cndmask_b32_e64 v58, v14, v58, s[52:53]
	v_cndmask_b32_e64 v59, v14, v59, s[52:53]
	v_cndmask_b32_e64 v60, v14, v60, s[54:55]
	v_cndmask_b32_e64 v61, v14, v61, s[54:55]
	v_cndmask_b32_e64 v62, v14, v62, s[56:57]
	v_cndmask_b32_e64 v63, v14, v63, s[56:57]
	v_max_f32_e32 v40, v56, v58
	v_max_f32_e32 v41, v57, v59
	v_max3_f32 v40, v40, v60, v62
	v_max3_f32 v41, v41, v61, v63
	s_nop 1
	v_max_f32_dpp v40, v40, v40 quad_perm:[1,0,3,2] row_mask:0xf bank_mask:0xf
	v_max_f32_dpp v41, v41, v41 quad_perm:[1,0,3,2] row_mask:0xf bank_mask:0xf
	s_nop 1
	v_max_f32_dpp v40, v40, v40 quad_perm:[2,3,0,1] row_mask:0xf bank_mask:0xf
	v_max_f32_dpp v41, v41, v41 quad_perm:[2,3,0,1] row_mask:0xf bank_mask:0xf
	s_nop 1
	v_max_f32_dpp v40, v40, v40 row_half_mirror row_mask:0xf bank_mask:0xf
	v_max_f32_dpp v41, v41, v41 row_half_mirror row_mask:0xf bank_mask:0xf
	s_nop 1
	v_max_f32_dpp v40, v40, v40 row_mirror row_mask:0xf bank_mask:0xf
	v_max_f32_dpp v41, v41, v41 row_mirror row_mask:0xf bank_mask:0xf
	s_nop 1
	v_mov_b32_e32 v42, v40
	v_mov_b32_e32 v43, v41
	s_nop 1
	v_permlane16_swap_b32_e32 v40, v42
	v_permlane16_swap_b32_e32 v41, v43
	v_max_f32_e32 v40, v40, v42
	v_max_f32_e32 v41, v41, v43
	v_mov_b32_e32 v42, v40
	v_mov_b32_e32 v43, v41
	s_nop 1
	v_permlane32_swap_b32_e32 v40, v42
	v_permlane32_swap_b32_e32 v41, v43
	v_max_f32_e32 v40, v40, v42
	v_max_f32_e32 v41, v41, v43
	v_sub_f32_e32 v56, v56, v40
	v_sub_f32_e32 v57, v57, v41
	v_sub_f32_e32 v58, v58, v40
	v_sub_f32_e32 v59, v59, v41
	v_sub_f32_e32 v60, v60, v40
	v_sub_f32_e32 v61, v61, v41
	v_sub_f32_e32 v62, v62, v40
	v_sub_f32_e32 v63, v63, v41
	v_mul_f32_e32 v56, 0x3fb8aa3b, v56
	v_mul_f32_e32 v57, 0x3fb8aa3b, v57
	v_mul_f32_e32 v58, 0x3fb8aa3b, v58
	v_mul_f32_e32 v59, 0x3fb8aa3b, v59
	v_mul_f32_e32 v60, 0x3fb8aa3b, v60
	v_mul_f32_e32 v61, 0x3fb8aa3b, v61
	v_mul_f32_e32 v62, 0x3fb8aa3b, v62
	v_mul_f32_e32 v63, 0x3fb8aa3b, v63
	v_exp_f32_e32 v56, v56
	v_exp_f32_e32 v57, v57
	v_exp_f32_e32 v58, v58
	v_exp_f32_e32 v59, v59
	v_exp_f32_e32 v60, v60
	v_exp_f32_e32 v61, v61
	v_exp_f32_e32 v62, v62
	v_exp_f32_e32 v63, v63
	s_nop 0
	v_add_f32_e32 v44, v56, v58
	v_add_f32_e32 v45, v57, v59
	v_add_f32_e32 v44, v44, v60
	v_add_f32_e32 v45, v45, v61
	v_add_f32_e32 v44, v44, v62
	v_add_f32_e32 v45, v45, v63
	s_nop 1
	v_add_f32_dpp v44, v44, v44 quad_perm:[1,0,3,2] row_mask:0xf bank_mask:0xf
	v_add_f32_dpp v45, v45, v45 quad_perm:[1,0,3,2] row_mask:0xf bank_mask:0xf
	s_nop 1
	v_add_f32_dpp v44, v44, v44 quad_perm:[2,3,0,1] row_mask:0xf bank_mask:0xf
	v_add_f32_dpp v45, v45, v45 quad_perm:[2,3,0,1] row_mask:0xf bank_mask:0xf
	s_nop 1
	v_add_f32_dpp v44, v44, v44 row_half_mirror row_mask:0xf bank_mask:0xf
	v_add_f32_dpp v45, v45, v45 row_half_mirror row_mask:0xf bank_mask:0xf
	s_nop 1
	v_add_f32_dpp v44, v44, v44 row_mirror row_mask:0xf bank_mask:0xf
	v_add_f32_dpp v45, v45, v45 row_mirror row_mask:0xf bank_mask:0xf
	s_nop 1
	v_mov_b32_e32 v42, v44
	v_mov_b32_e32 v43, v45
	s_nop 1
	v_permlane16_swap_b32_e32 v44, v42
	v_permlane16_swap_b32_e32 v45, v43
	v_add_f32_e32 v44, v44, v42
	v_add_f32_e32 v45, v45, v43
	v_mov_b32_e32 v42, v44
	v_mov_b32_e32 v43, v45
	s_nop 1
	v_permlane32_swap_b32_e32 v44, v42
	v_permlane32_swap_b32_e32 v45, v43
	v_add_f32_e32 v44, v44, v42
	v_add_f32_e32 v45, v45, v43
	v_rcp_f32_e32 v46, v44
	v_rcp_f32_e32 v47, v45
	s_nop 0
	v_fma_f32 v42, -v44, v46, 1.0
	v_fma_f32 v43, -v45, v47, 1.0
	v_fma_f32 v46, v42, v46, v46
	v_fma_f32 v47, v43, v47, v47
	v_mul_f32_e32 v56, v56, v46
	v_mul_f32_e32 v57, v57, v47
	v_mul_f32_e32 v58, v58, v46
	v_mul_f32_e32 v59, v59, v47
	v_mul_f32_e32 v60, v60, v46
	v_mul_f32_e32 v61, v61, v47
	v_mul_f32_e32 v62, v62, v46
	v_mul_f32_e32 v63, v63, v47
	v_cvt_pk_bf16_f32 v48, v56, v57
	v_cvt_pk_bf16_f32 v49, v58, v59
	v_cvt_pk_bf16_f32 v50, v60, v61
	v_cvt_pk_bf16_f32 v51, v62, v63
	ds_write_b16 v15, v48 offset:0
	ds_write_b16_d16_hi v15, v48 offset:512
	ds_write_b16 v15, v49 offset:128
	ds_write_b16_d16_hi v15, v49 offset:640
	ds_write_b16 v15, v50 offset:256
	ds_write_b16_d16_hi v15, v50 offset:768
	ds_write_b16 v15, v51 offset:384
	ds_write_b16_d16_hi v15, v51 offset:896
	v_lshlrev_b32_e32 v6, 12, v2
	v_lshl_or_b32 v6, v5, 9, v6
	v_lshl_or_b32 v6, v3, 4, v6
	v_lshlrev_b32_e32 v7, 9, v2
	v_lshl_or_b32 v7, v3, 4, v7
	v_lshlrev_b32_e32 v8, 9, v2
	v_lshl_or_b32 v8, v5, 6, v8
	v_lshl_or_b32 v8, v3, 3, v8
	v_mov_b32_e32 v40, 0
	v_mov_b32_e32 v41, 0
	v_mov_b32_e32 v42, 0
	v_mov_b32_e32 v43, 0
	v_mov_b32_e32 v44, 0
	v_mov_b32_e32 v45, 0
	v_mov_b32_e32 v46, 0
	v_mov_b32_e32 v47, 0
	v_mov_b32_e32 v48, 0
	v_mov_b32_e32 v49, 0
	v_mov_b32_e32 v50, 0
	v_mov_b32_e32 v51, 0
	v_mov_b32_e32 v52, 0
	v_mov_b32_e32 v53, 0
	v_mov_b32_e32 v54, 0
	v_mov_b32_e32 v55, 0
	global_load_dwordx4 v[64:67], v4, s[36:37]
	global_load_dwordx4 v[68:71], v4, s[36:37] offset:1024
	global_load_dwordx4 v[72:75], v4, s[36:37] offset:2048
	global_load_dwordx4 v[76:79], v4, s[36:37] offset:3072
	global_load_dwordx4 v[80:83], v9, s[36:37]
	global_load_dwordx4 v[84:87], v9, s[36:37] offset:1024
	global_load_dwordx4 v[88:91], v9, s[36:37] offset:2048
	global_load_dwordx4 v[92:95], v9, s[36:37] offset:3072
	global_load_dwordx4 v[96:99], v10, s[36:37]
	global_load_dwordx4 v[100:103], v10, s[36:37] offset:1024
	global_load_dwordx4 v[104:107], v10, s[36:37] offset:2048
	global_load_dwordx4 v[108:111], v10, s[36:37] offset:3072
	global_load_dwordx4 v[112:115], v11, s[36:37]
	global_load_dwordx4 v[116:119], v11, s[36:37] offset:1024
	global_load_dwordx4 v[120:123], v11, s[36:37] offset:2048
	global_load_dwordx4 v[124:127], v11, s[36:37] offset:3072
	global_load_dwordx4 v[128:131], v4, s[38:39]
	global_load_dwordx4 v[132:135], v4, s[38:39] offset:1024
	global_load_dwordx4 v[136:139], v4, s[38:39] offset:2048
	global_load_dwordx4 v[140:143], v4, s[38:39] offset:3072
	global_load_dwordx4 v[144:147], v9, s[38:39]
	global_load_dwordx4 v[148:151], v9, s[38:39] offset:1024
	global_load_dwordx4 v[152:155], v9, s[38:39] offset:2048
	global_load_dwordx4 v[156:159], v9, s[38:39] offset:3072
	global_load_dwordx4 v[160:163], v10, s[38:39]
	global_load_dwordx4 v[164:167], v10, s[38:39] offset:1024
	global_load_dwordx4 v[168:171], v10, s[38:39] offset:2048
	global_load_dwordx4 v[172:175], v10, s[38:39] offset:3072
	global_load_dwordx4 v[176:179], v11, s[38:39]
	global_load_dwordx4 v[180:183], v11, s[38:39] offset:1024
	global_load_dwordx4 v[184:187], v11, s[38:39] offset:2048
	global_load_dwordx4 v[188:191], v11, s[38:39] offset:3072
	global_load_dwordx4 v[192:195], v4, s[40:41]
	global_load_dwordx4 v[196:199], v4, s[40:41] offset:1024
	global_load_dwordx4 v[200:203], v4, s[40:41] offset:2048
	global_load_dwordx4 v[204:207], v4, s[40:41] offset:3072
	global_load_dwordx4 v[208:211], v9, s[40:41]
	global_load_dwordx4 v[212:215], v9, s[40:41] offset:1024
	global_load_dwordx4 v[216:219], v9, s[40:41] offset:2048
	global_load_dwordx4 v[220:223], v9, s[40:41] offset:3072
	global_load_dwordx4 v[224:227], v10, s[40:41]
	global_load_dwordx4 v[228:231], v10, s[40:41] offset:1024
	global_load_dwordx4 v[232:235], v10, s[40:41] offset:2048
	global_load_dwordx4 v[236:239], v10, s[40:41] offset:3072
	global_load_dwordx4 v[240:243], v11, s[40:41]
	global_load_dwordx4 v[244:247], v11, s[40:41] offset:1024
	global_load_dwordx4 v[248:251], v11, s[40:41] offset:2048
	global_load_dwordx4 v[252:255], v11, s[40:41] offset:3072
	s_waitcnt lgkmcnt(0)
	s_barrier
	s_waitcnt vmcnt(32)
	s_mov_b64 exec, s[58:59]
	ds_read_b128 v[40:43], v6 offset:0
	ds_read_b128 v[44:47], v6 offset:64
	ds_read_b128 v[48:51], v6 offset:128
	ds_read_b128 v[52:55], v6 offset:192
	s_mov_b64 exec, -1
	s_waitcnt lgkmcnt(0)
	v_mfma_f32_16x16x32_bf16 v[56:59], v[64:67], v[40:43], 0
	v_mfma_f32_16x16x32_bf16 v[60:63], v[96:99], v[40:43], 0
	v_mfma_f32_16x16x32_bf16 v[56:59], v[68:71], v[44:47], v[56:59]
	v_mfma_f32_16x16x32_bf16 v[60:63], v[100:103], v[44:47], v[60:63]
	v_mfma_f32_16x16x32_bf16 v[56:59], v[72:75], v[48:51], v[56:59]
	v_mfma_f32_16x16x32_bf16 v[60:63], v[104:107], v[48:51], v[60:63]
	v_mfma_f32_16x16x32_bf16 v[56:59], v[76:79], v[52:55], v[56:59]
	v_mfma_f32_16x16x32_bf16 v[60:63], v[108:111], v[52:55], v[60:63]
	s_mov_b64 exec, s[58:59]
	ds_read_b128 v[40:43], v6 offset:256
	ds_read_b128 v[44:47], v6 offset:320
	ds_read_b128 v[48:51], v6 offset:384
	ds_read_b128 v[52:55], v6 offset:448
	s_mov_b64 exec, -1
	s_waitcnt lgkmcnt(0)
	v_mfma_f32_16x16x32_bf16 v[56:59], v[80:83], v[40:43], v[56:59]
	v_mfma_f32_16x16x32_bf16 v[60:63], v[112:115], v[40:43], v[60:63]
	v_mfma_f32_16x16x32_bf16 v[56:59], v[84:87], v[44:47], v[56:59]
	v_mfma_f32_16x16x32_bf16 v[60:63], v[116:119], v[44:47], v[60:63]
	v_mfma_f32_16x16x32_bf16 v[56:59], v[88:91], v[48:51], v[56:59]
	v_mfma_f32_16x16x32_bf16 v[60:63], v[120:123], v[48:51], v[60:63]
	v_mfma_f32_16x16x32_bf16 v[56:59], v[92:95], v[52:55], v[56:59]
	v_mfma_f32_16x16x32_bf16 v[60:63], v[124:127], v[52:55], v[60:63]
	s_nop 9
	v_cvt_pk_bf16_f32 v48, v56, v57
	v_cvt_pk_bf16_f32 v49, v58, v59
	v_cvt_pk_bf16_f32 v50, v60, v61
	v_cvt_pk_bf16_f32 v51, v62, v63
	s_mov_b64 exec, s[58:59]
	ds_write_b64 v8, v[48:49] offset:8192
	ds_write_b64 v8, v[50:51] offset:8224
	s_mov_b64 exec, -1
	global_load_dwordx4 v[64:67], v4, s[42:43]
	global_load_dwordx4 v[68:71], v4, s[42:43] offset:1024
	global_load_dwordx4 v[72:75], v4, s[42:43] offset:2048
	global_load_dwordx4 v[76:79], v4, s[42:43] offset:3072
	global_load_dwordx4 v[80:83], v9, s[42:43]
	global_load_dwordx4 v[84:87], v9, s[42:43] offset:1024
	global_load_dwordx4 v[88:91], v9, s[42:43] offset:2048
	global_load_dwordx4 v[92:95], v9, s[42:43] offset:3072
	global_load_dwordx4 v[96:99], v10, s[42:43]
	global_load_dwordx4 v[100:103], v10, s[42:43] offset:1024
	global_load_dwordx4 v[104:107], v10, s[42:43] offset:2048
	global_load_dwordx4 v[108:111], v10, s[42:43] offset:3072
	global_load_dwordx4 v[112:115], v11, s[42:43]
	global_load_dwordx4 v[116:119], v11, s[42:43] offset:1024
	global_load_dwordx4 v[120:123], v11, s[42:43] offset:2048
	global_load_dwordx4 v[124:127], v11, s[42:43] offset:3072
	v_lshlrev_b32_e32 v15, 10, v2
	v_add_u32_e32 v15, v15, v12
	v_mov_b32_e32 v48, 0
	v_mov_b32_e32 v49, 0
	v_mov_b32_e32 v50, 0
	v_mov_b32_e32 v51, 0
	s_waitcnt lgkmcnt(0)
	s_barrier
	s_waitcnt vmcnt(32)
	s_mov_b64 exec, s[58:59]
	ds_read_b128 v[40:43], v7 offset:8192
	ds_read_b128 v[44:47], v7 offset:8256
	ds_read_b128 v[48:51], v7 offset:8320
	ds_read_b128 v[52:55], v7 offset:8384
	s_mov_b64 exec, -1
	s_waitcnt lgkmcnt(0)
	v_mfma_f32_16x16x32_bf16 v[56:59], v[128:131], v[40:43], 0
	v_mfma_f32_16x16x32_bf16 v[60:63], v[160:163], v[40:43], 0
	v_mfma_f32_16x16x32_bf16 v[56:59], v[132:135], v[44:47], v[56:59]
	v_mfma_f32_16x16x32_bf16 v[60:63], v[164:167], v[44:47], v[60:63]
	v_mfma_f32_16x16x32_bf16 v[56:59], v[136:139], v[48:51], v[56:59]
	v_mfma_f32_16x16x32_bf16 v[60:63], v[168:171], v[48:51], v[60:63]
	v_mfma_f32_16x16x32_bf16 v[56:59], v[140:143], v[52:55], v[56:59]
	v_mfma_f32_16x16x32_bf16 v[60:63], v[172:175], v[52:55], v[60:63]
	s_mov_b64 exec, s[58:59]
	ds_read_b128 v[40:43], v7 offset:8448
	ds_read_b128 v[44:47], v7 offset:8512
	ds_read_b128 v[48:51], v7 offset:8576
	ds_read_b128 v[52:55], v7 offset:8640
	s_mov_b64 exec, -1
	s_waitcnt lgkmcnt(0)
	v_mfma_f32_16x16x32_bf16 v[56:59], v[144:147], v[40:43], v[56:59]
	v_mfma_f32_16x16x32_bf16 v[60:63], v[176:179], v[40:43], v[60:63]
	v_mfma_f32_16x16x32_bf16 v[56:59], v[148:151], v[44:47], v[56:59]
	v_mfma_f32_16x16x32_bf16 v[60:63], v[180:183], v[44:47], v[60:63]
	v_mfma_f32_16x16x32_bf16 v[56:59], v[152:155], v[48:51], v[56:59]
	v_mfma_f32_16x16x32_bf16 v[60:63], v[184:187], v[48:51], v[60:63]
	v_mfma_f32_16x16x32_bf16 v[56:59], v[156:159], v[52:55], v[56:59]
	v_mfma_f32_16x16x32_bf16 v[60:63], v[188:191], v[52:55], v[60:63]
	s_nop 9
	v_add_f32_e32 v56, v56, v16
	v_add_f32_e32 v57, v57, v17
	v_add_f32_e32 v58, v58, v18
	v_add_f32_e32 v59, v59, v19
	v_add_f32_e32 v60, v60, v20
	v_add_f32_e32 v61, v61, v21
	v_add_f32_e32 v62, v62, v22
	v_add_f32_e32 v63, v63, v23
	v_add_f32_e32 v24, v56, v24
	v_add_f32_e32 v25, v57, v25
	v_add_f32_e32 v26, v58, v26
	v_add_f32_e32 v27, v59, v27
	v_add_f32_e32 v28, v60, v28
	v_add_f32_e32 v29, v61, v29
	v_add_f32_e32 v30, v62, v30
	v_add_f32_e32 v31, v63, v31
	s_mov_b64 exec, s[58:59]
	ds_write_b128 v15, v[24:27] offset:10240
	ds_write_b128 v15, v[28:31] offset:10304
	s_mov_b64 exec, -1
	global_load_dwordx4 v[16:19], v12, s[20:21]
	global_load_dwordx4 v[20:23], v12, s[20:21] offset:64
	s_waitcnt lgkmcnt(0)
	s_barrier
	s_cmp_gt_u32 s26, 1
	s_cbranch_scc1 .Lnp_ln_done
	s_lshl_b32 s48, s26, 10
	v_add_u32_e32 v40, s48, v4
	ds_read_b128 v[44:47], v40 offset:10240
	s_waitcnt lgkmcnt(0)
	v_add_f32_e32 v41, v44, v45
	v_add_f32_e32 v41, v41, v46
	v_add_f32_e32 v41, v41, v47
	s_nop 1
	v_add_f32_dpp v41, v41, v41 quad_perm:[1,0,3,2] row_mask:0xf bank_mask:0xf
	s_nop 1
	v_add_f32_dpp v41, v41, v41 quad_perm:[2,3,0,1] row_mask:0xf bank_mask:0xf
	s_nop 1
	v_add_f32_dpp v41, v41, v41 row_half_mirror row_mask:0xf bank_mask:0xf
	s_nop 1
	v_add_f32_dpp v41, v41, v41 row_mirror row_mask:0xf bank_mask:0xf
	s_nop 1
	v_mov_b32_e32 v42, v41
	s_nop 1
	v_permlane16_swap_b32_e32 v41, v42
	v_add_f32_e32 v41, v41, v42
	v_mov_b32_e32 v42, v41
	s_nop 1
	v_permlane32_swap_b32_e32 v41, v42
	v_add_f32_e32 v41, v41, v42
	v_mul_f32_e32 v41, 0x3b800000, v41
	v_sub_f32_e32 v44, v44, v41
	v_sub_f32_e32 v45, v45, v41
	v_sub_f32_e32 v46, v46, v41
	v_sub_f32_e32 v47, v47, v41
	v_mul_f32_e32 v43, v44, v44
	v_fmac_f32_e32 v43, v45, v45
	v_fmac_f32_e32 v43, v46, v46
	v_fmac_f32_e32 v43, v47, v47
	s_nop 1
	v_add_f32_dpp v43, v43, v43 quad_perm:[1,0,3,2] row_mask:0xf bank_mask:0xf
	s_nop 1
	v_add_f32_dpp v43, v43, v43 quad_perm:[2,3,0,1] row_mask:0xf bank_mask:0xf
	s_nop 1
	v_add_f32_dpp v43, v43, v43 row_half_mirror row_mask:0xf bank_mask:0xf
	s_nop 1
	v_add_f32_dpp v43, v43, v43 row_mirror row_mask:0xf bank_mask:0xf
	s_nop 1
	v_mov_b32_e32 v42, v43
	s_nop 1
	v_permlane16_swap_b32_e32 v43, v42
	v_add_f32_e32 v43, v43, v42
	v_mov_b32_e32 v42, v43
	s_nop 1
	v_permlane32_swap_b32_e32 v43, v42
	v_add_f32_e32 v43, v43, v42
	v_mov_b32_e32 v42, 0x3727c5ac
	v_fmac_f32_e32 v42, 0x3b800000, v43
	v_rsq_f32_e32 v42, v42
	s_nop 0
	v_mul_f32_e32 v44, v44, v42
	v_mul_f32_e32 v45, v45, v42
	v_mul_f32_e32 v46, v46, v42
	v_mul_f32_e32 v47, v47, v42
	v_fma_f32 v44, v44, v32, v36
	v_fma_f32 v45, v45, v33, v37
	v_fma_f32 v46, v46, v34, v38
	v_fma_f32 v47, v47, v35, v39
	v_cvt_pk_bf16_f32 v48, v44, v45
	v_cvt_pk_bf16_f32 v49, v46, v47
	s_lshl_b32 s48, s26, 9
	v_lshlrev_b32_e32 v40, 3, v1
	v_add_u32_e32 v40, s48, v40
	ds_write_b64 v40, v[48:49] offset:8192
	v_mov_b32_e32 v40, 0
	v_mov_b32_e32 v41, 0
	v_mov_b32_e32 v42, 0
	v_mov_b32_e32 v43, 0
	v_mov_b32_e32 v44, 0
	v_mov_b32_e32 v45, 0
	v_mov_b32_e32 v46, 0
	v_mov_b32_e32 v47, 0
	v_mov_b32_e32 v48, 0
	v_mov_b32_e32 v49, 0
	v_mov_b32_e32 v50, 0
	v_mov_b32_e32 v51, 0

	.amdhsa_kernel _Z16node_post_kernelPKfS0_PKtS0_S2_S0_S0_S0_S0_S0_Pf
		.amdhsa_group_segment_fixed_size 12288
		.amdhsa_private_segment_fixed_size 0
		.amdhsa_kernarg_size 88
		.amdhsa_user_sgpr_count 2
		.amdhsa_user_sgpr_dispatch_ptr 0
		.amdhsa_user_sgpr_queue_ptr 0
		.amdhsa_user_sgpr_kernarg_segment_ptr 1
		.amdhsa_user_sgpr_dispatch_id 0
		.amdhsa_user_sgpr_kernarg_preload_length 0
		.amdhsa_user_sgpr_kernarg_preload_offset 0
		.amdhsa_user_sgpr_private_segment_size 0
		.amdhsa_uses_dynamic_stack 0
		.amdhsa_enable_private_segment 0
		.amdhsa_system_sgpr_workgroup_id_x 1
		.amdhsa_system_sgpr_workgroup_id_y 0
		.amdhsa_system_sgpr_workgroup_id_z 0
		.amdhsa_system_sgpr_workgroup_info 0
		.amdhsa_system_vgpr_workitem_id 0
		.amdhsa_next_free_vgpr 256
		.amdhsa_next_free_sgpr 102
		.amdhsa_accum_offset 256
		.amdhsa_reserve_vcc 1
		.amdhsa_float_round_mode_32 0
		.amdhsa_float_round_mode_16_64 0
		.amdhsa_float_denorm_mode_32 3
		.amdhsa_float_denorm_mode_16_64 3
		.amdhsa_dx10_clamp 1
		.amdhsa_ieee_mode 1
		.amdhsa_fp16_overflow 0
		.amdhsa_tg_split 0
		.amdhsa_exception_fp_ieee_invalid_op 0
		.amdhsa_exception_fp_denorm_src 0
		.amdhsa_exception_fp_ieee_div_zero 0
		.amdhsa_exception_fp_ieee_overflow 0
		.amdhsa_exception_fp_ieee_underflow 0
		.amdhsa_exception_fp_ieee_inexact 0
		.amdhsa_exception_int_div_zero 0
	.end_amdhsa_kernel

amdhsa.kernels:
  - .agpr_count:     0
    .args:
      - .actual_access:  read_only
        .address_space:  global
        .offset:         0
        .size:           8
        .value_kind:     global_buffer
      - .actual_access:  read_only
        .address_space:  global
        .offset:         8
        .size:           8
        .value_kind:     global_buffer
      - .actual_access:  read_only
        .address_space:  global
        .offset:         16
        .size:           8
        .value_kind:     global_buffer
      - .actual_access:  read_only
        .address_space:  global
        .offset:         24
        .size:           8
        .value_kind:     global_buffer
      - .actual_access:  read_only
        .address_space:  global
        .offset:         32
        .size:           8
        .value_kind:     global_buffer
      - .actual_access:  read_only
        .address_space:  global
        .offset:         40
        .size:           8
        .value_kind:     global_buffer
      - .actual_access:  read_only
        .address_space:  global
        .offset:         48
        .size:           8
        .value_kind:     global_buffer
      - .actual_access:  read_only
        .address_space:  global
        .offset:         56
        .size:           8
        .value_kind:     global_buffer
      - .actual_access:  read_only
        .address_space:  global
        .offset:         64
        .size:           8
        .value_kind:     global_buffer
      - .actual_access:  read_only
        .address_space:  global
        .offset:         72
        .size:           8
        .value_kind:     global_buffer
      - .actual_access:  read_only
        .address_space:  global
        .offset:         80
        .size:           8
        .value_kind:     global_buffer
      - .actual_access:  write_only
        .address_space:  global
        .offset:         88
        .size:           8
        .value_kind:     global_buffer
      - .actual_access:  write_only
        .address_space:  global
        .offset:         96
        .size:           8
        .value_kind:     global_buffer
      - .actual_access:  read_only
        .address_space:  global
        .offset:         104
        .size:           8
        .value_kind:     global_buffer
      - .actual_access:  read_only
        .address_space:  global
        .offset:         112
        .size:           8
        .value_kind:     global_buffer
      - .actual_access:  read_only
        .address_space:  global
        .offset:         120
        .size:           8
        .value_kind:     global_buffer
      - .actual_access:  read_only
        .address_space:  global
        .offset:         128
        .size:           8
        .value_kind:     global_buffer
      - .actual_access:  read_only
        .address_space:  global
        .offset:         136
        .size:           8
        .value_kind:     global_buffer
      - .actual_access:  read_only
        .address_space:  global
        .offset:         144
        .size:           8
        .value_kind:     global_buffer
      - .actual_access:  write_only
        .address_space:  global
        .offset:         152
        .size:           8
        .value_kind:     global_buffer
      - .actual_access:  write_only
        .address_space:  global
        .offset:         160
        .size:           8
        .value_kind:     global_buffer
      - .actual_access:  write_only
        .address_space:  global
        .offset:         168
        .size:           8
        .value_kind:     global_buffer
      - .actual_access:  read_only
        .address_space:  global
        .offset:         176
        .size:           8
        .value_kind:     global_buffer
      - .actual_access:  read_only
        .address_space:  global
        .offset:         184
        .size:           8
        .value_kind:     global_buffer
      - .actual_access:  read_only
        .address_space:  global
        .offset:         192
        .size:           8
        .value_kind:     global_buffer
      - .actual_access:  write_only
        .address_space:  global
        .offset:         200
        .size:           8
        .value_kind:     global_buffer
    .group_segment_fixed_size: 40960
    .kernarg_segment_align: 8
    .kernarg_segment_size: 208
    .language:       OpenCL C
    .language_version:
      - 2
      - 0
    .max_flat_workgroup_size: 256
    .name:           _Z10pre_kernelPKfS0_S0_S0_S0_S0_S0_S0_S0_S0_S0_PtPfS0_S0_S0_S0_S0_S0_S2_S2_S2_S0_S0_S0_S1_
    .private_segment_fixed_size: 0
    .sgpr_count:     106
    .sgpr_spill_count: 0
    .symbol:         _Z10pre_kernelPKfS0_S0_S0_S0_S0_S0_S0_S0_S0_S0_PtPfS0_S0_S0_S0_S0_S0_S2_S2_S2_S0_S0_S0_S1_.kd
    .uniform_work_group_size: 1
    .uses_dynamic_stack: false
    .vgpr_count:     128
    .vgpr_spill_count: 0
    .wavefront_size: 64
  - .agpr_count:     0
    .args:
      - .actual_access:  read_only
        .address_space:  global
        .offset:         0
        .size:           8
        .value_kind:     global_buffer
      - .address_space:  global
        .offset:         8
        .size:           8
        .value_kind:     global_buffer
      - .address_space:  global
        .offset:         16
        .size:           8
        .value_kind:     global_buffer
      - .address_space:  global
        .offset:         24
        .size:           8
        .value_kind:     global_buffer
      - .address_space:  global
        .offset:         32
        .size:           8
        .value_kind:     global_buffer
      - .actual_access:  write_only
        .address_space:  global
        .offset:         40
        .size:           8
        .value_kind:     global_buffer
      - .actual_access:  write_only
        .address_space:  global
        .offset:         48
        .size:           8
        .value_kind:     global_buffer
    .group_segment_fixed_size: 79872
    .kernarg_segment_align: 8
    .kernarg_segment_size: 56
    .language:       OpenCL C
    .language_version:
      - 2
      - 0
    .max_flat_workgroup_size: 256
    .name:           _Z11edge_kernelPKfPK15HIP_vector_typeIjLj4EES0_S0_S4_PfS5_
    .private_segment_fixed_size: 0
    .sgpr_count:     26
    .sgpr_spill_count: 0
    .symbol:         _Z11edge_kernelPKfPK15HIP_vector_typeIjLj4EES0_S0_S4_PfS5_.kd
    .uniform_work_group_size: 1
    .uses_dynamic_stack: false
    .vgpr_count:     256
    .vgpr_spill_count: 0
    .wavefront_size: 64
  - .agpr_count:     0
    .args:
      - .actual_access:  read_only
        .address_space:  global
        .offset:         0
        .size:           8
        .value_kind:     global_buffer
      - .actual_access:  read_only
        .address_space:  global
        .offset:         8
        .size:           8
        .value_kind:     global_buffer
      - .actual_access:  read_only
        .address_space:  global
        .offset:         16
        .size:           8
        .value_kind:     global_buffer
      - .actual_access:  read_only
        .address_space:  global
        .offset:         24
        .size:           8
        .value_kind:     global_buffer
      - .actual_access:  read_only
        .address_space:  global
        .offset:         32
        .size:           8
        .value_kind:     global_buffer
      - .actual_access:  read_only
        .address_space:  global
        .offset:         40
        .size:           8
        .value_kind:     global_buffer
      - .actual_access:  read_only
        .address_space:  global
        .offset:         48
        .size:           8
        .value_kind:     global_buffer
      - .actual_access:  read_only
        .address_space:  global
        .offset:         56
        .size:           8
        .value_kind:     global_buffer
      - .actual_access:  read_only
        .address_space:  global
        .offset:         64
        .size:           8
        .value_kind:     global_buffer
      - .actual_access:  read_only
        .address_space:  global
        .offset:         72
        .size:           8
        .value_kind:     global_buffer
      - .actual_access:  write_only
        .address_space:  global
        .offset:         80
        .size:           8
        .value_kind:     global_buffer
    .group_segment_fixed_size: 12288
    .kernarg_segment_align: 8
    .kernarg_segment_size: 88
    .language:       OpenCL C
    .language_version:
      - 2
      - 0
    .max_flat_workgroup_size: 512
    .name:           _Z16node_post_kernelPKfS0_PKtS0_S2_S0_S0_S0_S0_S0_Pf
    .private_segment_fixed_size: 0
    .sgpr_count:     108
    .sgpr_spill_count: 0
    .symbol:         _Z16node_post_kernelPKfS0_PKtS0_S2_S0_S0_S0_S0_S0_Pf.kd
    .uniform_work_group_size: 1
    .uses_dynamic_stack: false
    .vgpr_count:     256
    .vgpr_spill_count: 0
    .wavefront_size: 64
